# attention: K/V staging writes + next loads moved after the QK MFMAs; expert GEMM loops: dropped the B-read drain before the A reads
# baseline (speedup 1.0000x reference)
; #define LAS __attribute__((address_space(3)))
; __device__ __forceinline__ void phase_attn(Frame& F) {
;     ...
;     for (; jl < PER_X; jl += G8) {
;         lds_barrier();
;         LAS unsigned char* kb = F.lds + buf * ABUF;
;         const bf16x8 q0 = qn0, q1 = qn1;
;         {
;             LAS unsigned char* ob = F.lds + (buf ^ 1) * ABUF;
; #pragma unroll
;             for (int jj = 0; jj < 4; ++jj) { const int ch = tid + 512 * jj, row = ch >> 3, c16 = ch & 7;
;                 *(LAS u32x4*)(ob + row * ATT_ROWB + c16 * 16) = kr[jj]; *(LAS u32x4*)(ob + ATT_VOFF + row * ATT_ROWB + c16 * 16) = vr[jj]; }
;         }
;         const AttnUnit nu = un;
;         un = attn_decode(x8 * PER_X + (jl + 2 * G8 < jlast ? jl + 2 * G8 : jlast)); attn_issue(qkv, un, tid, kr, vr);
;         { const char* qb = (const char*)qkv + (((size_t)nu.b * SEQ + nu.r) * NPROJ + nu.h * 64) * 2; const unsigned qo = __umul24((unsigned)(128 * nu.n + ql), (unsigned)nu.d * (NPROJ * 2)) + 16u * fq;
;           qn0 = *(const bf16x8*)(qb + qo); qn1 = *(const bf16x8*)(qb + qo + 64); }
;         const unsigned qrow = __umul24((unsigned)(128 * cu.n + ql), (unsigned)cu.d);
;         const float c1 = 0.125f * LOG2E;
;         const float nc2 = -__builtin_amdgcn_exp2f(-(float)(cu.h + 1)) * (float)cu.d * LOG2E;
;         const bool first = cu.n == 0;
;         f32x4 St[9];
;         const f32x4 eb = (f32x4){ef[0], ef[1], ef[2], ef[3]} * nc2;
;         float mx = -INFINITY;
;         bf16x8 kf[9][2];
; #pragma unroll
;         for (int T = 0; T < 9; ++T) { LAS unsigned char* ka = kb + (16 * (w + T) + fr) * ATT_ROWB + fq * 16; kf[T][0] = *(LAS bf16x8*)ka; kf[T][1] = *(LAS bf16x8*)(ka + 64); }
;         __builtin_amdgcn_sched_barrier(0);
; #pragma unroll
;         for (int T = 0; T < 9; ++T) {
;             f32x4 sa = (f32x4){0.f, 0.f, 0.f, 0.f};
;             sa = __builtin_amdgcn_mfma_f32_16x16x32_bf16(kf[T][0], q0, sa, 0, 0, 0);
;             sa = __builtin_amdgcn_mfma_f32_16x16x32_bf16(kf[T][1], q1, sa, 0, 0, 0);
;             const float kT = (!first || w + T >= 8) ? nc2 * (float)(128 - 16 * T) : -INFINITY;
;             sa = sa * c1 + (eb + kT);
; #pragma unroll
;             for (int rg = 0; rg < 4; ++rg) {
;                 if (T == 0) sa[rg] = ef[rg] <= 0.f ? sa[rg] : -INFINITY;
;                 if (T == 8) sa[rg] = ef[rg] >= 0.f ? sa[rg] : -INFINITY;
;             }
;             St[T] = sa;
.LBB0_304:
	s_mul_i32 s37, s79, 0x12000
	s_add_i32 s85, s37, 0
	s_waitcnt vmcnt(3)
	v_mov_b64_e32 v[48:49], v[4:5]
	v_mov_b64_e32 v[46:47], v[2:3]
	v_mov_b64_e32 v[44:45], v[8:9]
	v_mov_b64_e32 v[42:43], v[6:7]
	s_lshl_b32 s65, 1, s35
	s_waitcnt lgkmcnt(0)
	s_barrier
	s_add_i32 s37, s30, 1
	v_cvt_f32_u32_e32 v54, s37
	v_cvt_f32_u32_e32 v55, s65
	v_add_u32_e32 v110, s85, v82
	v_add_u32_e32 v58, v110, v90
	v_exp_f32_e64 v54, -v54
	v_add_u32_e32 v66, v110, v91
	v_add_u32_e32 v74, v110, v92
	v_add_u32_e32 v111, v110, v93
	v_mul_f32_e32 v79, v55, v54
	ds_read_b128 v[54:57], v58
	ds_read_b128 v[58:61], v58 offset:64
	ds_read_b128 v[62:65], v66
	ds_read_b128 v[66:69], v66 offset:64
	ds_read_b128 v[70:73], v74
	ds_read_b128 v[74:77], v74 offset:64
	ds_read_b128 v[112:115], v111
	ds_read_b128 v[116:119], v111 offset:64
	v_add_u32_e32 v111, v110, v94
	ds_read_b128 v[120:123], v111
	ds_read_b128 v[124:127], v111 offset:64
	v_add_u32_e32 v111, v110, v95
	ds_read_b128 v[128:131], v111
	ds_read_b128 v[132:135], v111 offset:64
	v_add_u32_e32 v111, v110, v96
	ds_read_b128 v[136:139], v111
	ds_read_b128 v[140:143], v111 offset:64
	v_add_u32_e32 v111, v110, v97
	v_add_u32_e32 v110, v110, v98
	ds_read_b128 v[144:147], v111
	ds_read_b128 v[148:151], v111 offset:64
	ds_read_b128 v[152:155], v110
	ds_read_b128 v[156:159], v110 offset:64
	s_cmp_lg_u32 s64, 0
	v_lshl_add_u32 v78, s64, 7, v86
	s_cselect_b64 s[64:65], -1, 0
	v_mul_f32_e32 v160, 0xbfb8aa3b, v79
	v_and_b32_e32 v110, 0xffffff, v78
	s_waitcnt lgkmcnt(14)
	v_mfma_f32_16x16x32_bf16 v[54:57], v[54:57], v[46:49], 0
	v_mul_f32_e32 v78, 0x43000000, v160
	s_or_b64 vcc, s[64:65], s[38:39]
	v_cndmask_b32_e32 v78, v109, v78, vcc
	v_mfma_f32_16x16x32_bf16 v[54:57], v[58:61], v[42:45], v[54:57]
	v_fma_f32 v162, v50, v160, v78
	v_fma_f32 v163, v51, v160, v78
	v_pk_fma_f32 v[78:79], v[52:53], v[160:161], v[78:79] op_sel_hi:[1,0,0]
	s_or_b64 vcc, s[64:65], s[40:41]
	s_nop 3
	v_pk_fma_f32 v[56:57], v[56:57], s[56:57], v[78:79] op_sel_hi:[1,0,1]
	v_pk_fma_f32 v[54:55], v[54:55], s[56:57], v[162:163] op_sel_hi:[1,0,1]
	v_cndmask_b32_e64 v164, v109, v56, s[10:11]
	v_cndmask_b32_e64 v162, v109, v54, s[6:7]
	v_cndmask_b32_e64 v163, v109, v55, s[8:9]
	v_cndmask_b32_e64 v165, v109, v57, s[12:13]
	v_mfma_f32_16x16x32_bf16 v[54:57], v[62:65], v[46:49], 0
	v_max_f32_e32 v58, v162, v163
	v_max_f32_e32 v59, v164, v165
	v_max3_f32 v62, v58, v59, s78
	v_mfma_f32_16x16x32_bf16 v[54:57], v[66:69], v[42:45], v[54:57]
	v_mul_f32_e32 v58, 0x42e00000, v160
	v_cndmask_b32_e32 v58, v109, v58, vcc
	v_pk_fma_f32 v[60:61], v[50:51], v[160:161], v[58:59] op_sel_hi:[1,0,0]
	v_pk_fma_f32 v[58:59], v[52:53], v[160:161], v[58:59] op_sel_hi:[1,0,0]
	s_or_b64 vcc, s[64:65], s[42:43]
	s_nop 2
	v_pk_fma_f32 v[166:167], v[56:57], s[56:57], v[58:59] op_sel_hi:[1,0,1]
	s_waitcnt lgkmcnt(13)
	v_mfma_f32_16x16x32_bf16 v[56:59], v[70:73], v[46:49], 0
	v_fma_f32 v78, v54, s56, v60
	v_fma_f32 v79, v55, s56, v61
	v_max_f32_e32 v54, v166, v167
	v_max3_f32 v63, v78, v79, v54
	s_waitcnt lgkmcnt(12)
	v_mfma_f32_16x16x32_bf16 v[54:57], v[74:77], v[42:45], v[56:59]
	s_nop 2
	v_mul_f32_e32 v58, 0x42c00000, v160
	v_cndmask_b32_e32 v58, v109, v58, vcc
	v_pk_fma_f32 v[60:61], v[50:51], v[160:161], v[58:59] op_sel_hi:[1,0,0]
	v_pk_fma_f32 v[58:59], v[52:53], v[160:161], v[58:59] op_sel_hi:[1,0,0]
	s_nop 0
	v_pk_fma_f32 v[76:77], v[54:55], s[56:57], v[60:61] op_sel_hi:[1,0,1]
	v_pk_fma_f32 v[74:75], v[56:57], s[56:57], v[58:59] op_sel_hi:[1,0,1]
	s_waitcnt lgkmcnt(11)
	v_mfma_f32_16x16x32_bf16 v[54:57], v[112:115], v[46:49], 0
	v_max_f32_e32 v58, v74, v75
	v_max3_f32 v58, v76, v77, v58
	v_max3_f32 v62, v62, v63, v58
	s_waitcnt lgkmcnt(10)
	v_mfma_f32_16x16x32_bf16 v[54:57], v[116:119], v[42:45], v[54:57]
	v_mul_f32_e32 v58, 0x42a00000, v160
	s_or_b64 vcc, s[64:65], s[44:45]
	v_cndmask_b32_e32 v58, v109, v58, vcc
	v_pk_fma_f32 v[60:61], v[50:51], v[160:161], v[58:59] op_sel_hi:[1,0,0]
	v_pk_fma_f32 v[58:59], v[52:53], v[160:161], v[58:59] op_sel_hi:[1,0,0]
	s_nop 2
	v_pk_fma_f32 v[72:73], v[54:55], s[56:57], v[60:61] op_sel_hi:[1,0,1]
	v_pk_fma_f32 v[70:71], v[56:57], s[56:57], v[58:59] op_sel_hi:[1,0,1]
	s_waitcnt lgkmcnt(9)
	v_mfma_f32_16x16x32_bf16 v[56:59], v[120:123], v[46:49], 0
	v_max_f32_e32 v54, v70, v71
	v_max3_f32 v63, v72, v73, v54
	s_or_b64 vcc, s[64:65], s[46:47]
	s_waitcnt lgkmcnt(8)
	v_mfma_f32_16x16x32_bf16 v[54:57], v[124:127], v[42:45], v[56:59]
	s_nop 2
	v_mul_f32_e32 v58, 0x42800000, v160
	v_cndmask_b32_e32 v58, v109, v58, vcc
	v_pk_fma_f32 v[60:61], v[50:51], v[160:161], v[58:59] op_sel_hi:[1,0,0]
	v_pk_fma_f32 v[58:59], v[52:53], v[160:161], v[58:59] op_sel_hi:[1,0,0]
	s_nop 0
	v_pk_fma_f32 v[68:69], v[54:55], s[56:57], v[60:61] op_sel_hi:[1,0,1]
	v_pk_fma_f32 v[66:67], v[56:57], s[56:57], v[58:59] op_sel_hi:[1,0,1]
	s_waitcnt lgkmcnt(7)
	v_mfma_f32_16x16x32_bf16 v[54:57], v[128:131], v[46:49], 0
	v_max_f32_e32 v58, v66, v67
	v_max3_f32 v58, v68, v69, v58
	v_max3_f32 v111, v62, v63, v58
	s_waitcnt lgkmcnt(6)
	v_mfma_f32_16x16x32_bf16 v[54:57], v[132:135], v[42:45], v[54:57]
	v_mul_f32_e32 v58, 0x42400000, v160
	s_or_b64 vcc, s[64:65], s[48:49]
	v_cndmask_b32_e32 v58, v109, v58, vcc
	v_pk_fma_f32 v[60:61], v[50:51], v[160:161], v[58:59] op_sel_hi:[1,0,0]
	v_pk_fma_f32 v[58:59], v[52:53], v[160:161], v[58:59] op_sel_hi:[1,0,0]
	s_nop 2
	v_pk_fma_f32 v[64:65], v[54:55], s[56:57], v[60:61] op_sel_hi:[1,0,1]
	v_pk_fma_f32 v[62:63], v[56:57], s[56:57], v[58:59] op_sel_hi:[1,0,1]
	s_waitcnt lgkmcnt(5)
	v_mfma_f32_16x16x32_bf16 v[56:59], v[136:139], v[46:49], 0
	v_max_f32_e32 v54, v62, v63
	v_max3_f32 v112, v64, v65, v54
	s_or_b64 vcc, s[64:65], s[50:51]
	s_waitcnt lgkmcnt(4)
; __device__ __forceinline__ void phase_attn(Frame& F) {
;     ...
;             LAS unsigned char* ob = F.lds + (buf ^ 1) * ABUF;
; #pragma unroll
;             for (int jj = 0; jj < 4; ++jj) { const int ch = tid + 512 * jj, row = ch >> 3, c16 = ch & 7;
;                 *(LAS u32x4*)(ob + row * ATT_ROWB + c16 * 16) = kr[jj]; *(LAS u32x4*)(ob + ATT_VOFF + row * ATT_ROWB + c16 * 16) = vr[jj]; }
;         }
;         const AttnUnit nu = un;
;         un = attn_decode(x8 * PER_X + (jl + 2 * G8 < jlast ? jl + 2 * G8 : jlast)); attn_issue(qkv, un, tid, kr, vr);
;         { const char* qb = (const char*)qkv + (((size_t)nu.b * SEQ + nu.r) * NPROJ + nu.h * 64) * 2; const unsigned qo = __umul24((unsigned)(128 * nu.n + ql), (unsigned)nu.d * (NPROJ * 2)) + 16u * fq;
;           qn0 = *(const bf16x8*)(qb + qo); qn1 = *(const bf16x8*)(qb + qo + 64); }
;         const unsigned qrow = __umul24((unsigned)(128 * cu.n + ql), (unsigned)cu.d);
;         const float c1 = 0.125f * LOG2E;
;         const float nc2 = -__builtin_amdgcn_exp2f(-(float)(cu.h + 1)) * (float)cu.d * LOG2E;
;         const bool first = cu.n == 0;
;         f32x4 St[9];
;         const f32x4 eb = (f32x4){ef[0], ef[1], ef[2], ef[3]} * nc2;
;         float mx = -INFINITY;
;         bf16x8 kf[9][2];
; #pragma unroll
;         for (int T = 0; T < 9; ++T) { LAS unsigned char* ka = kb + (16 * (w + T) + fr) * ATT_ROWB + fq * 16; kf[T][0] = *(LAS bf16x8*)ka; kf[T][1] = *(LAS bf16x8*)(ka + 64); }
;         __builtin_amdgcn_sched_barrier(0);
; #pragma unroll
;         for (int T = 0; T < 9; ++T) {
;             f32x4 sa = (f32x4){0.f, 0.f, 0.f, 0.f};
;             sa = __builtin_amdgcn_mfma_f32_16x16x32_bf16(kf[T][0], q0, sa, 0, 0, 0);
;             sa = __builtin_amdgcn_mfma_f32_16x16x32_bf16(kf[T][1], q1, sa, 0, 0, 0);
;             const float kT = (!first || w + T >= 8) ? nc2 * (float)(128 - 16 * T) : -INFINITY;
;             sa = sa * c1 + (eb + kT);
; #pragma unroll
;             for (int rg = 0; rg < 4; ++rg) {
;                 if (T == 0) sa[rg] = ef[rg] <= 0.f ? sa[rg] : -INFINITY;
;                 if (T == 8) sa[rg] = ef[rg] >= 0.f ? sa[rg] : -INFINITY;
;             }
;             St[T] = sa;
;             mx = fmaxf(mx, fmaxf(fmaxf(sa[0], sa[1]), fmaxf(sa[2], sa[3])));
;         }
;         mx = fmaxf(mx, __shfl_xor(mx, 16)); mx = fmaxf(mx, __shfl_xor(mx, 32));
;         f32x4 lv = (f32x4){0.f, 0.f, 0.f, 0.f};
	v_mfma_f32_16x16x32_bf16 v[54:57], v[140:143], v[42:45], v[56:59]
	s_nop 2
	v_mul_f32_e32 v58, 0x42000000, v160
	v_cndmask_b32_e32 v58, v109, v58, vcc
	v_pk_fma_f32 v[60:61], v[50:51], v[160:161], v[58:59] op_sel_hi:[1,0,0]
	v_pk_fma_f32 v[58:59], v[52:53], v[160:161], v[58:59] op_sel_hi:[1,0,0]
	s_nop 0
	v_pk_fma_f32 v[60:61], v[54:55], s[56:57], v[60:61] op_sel_hi:[1,0,1]
	v_pk_fma_f32 v[58:59], v[56:57], s[56:57], v[58:59] op_sel_hi:[1,0,1]
	s_waitcnt lgkmcnt(3)
	v_mfma_f32_16x16x32_bf16 v[54:57], v[144:147], v[46:49], 0
	v_max_f32_e32 v113, v58, v59
	v_max3_f32 v113, v60, v61, v113
	v_max3_f32 v111, v111, v112, v113
	s_waitcnt lgkmcnt(1)
	v_mfma_f32_16x16x32_bf16 v[46:49], v[152:155], v[46:49], 0
	s_or_b64 vcc, s[64:65], s[52:53]
	v_add_u32_e32 v144, s85, v89
	v_add_u32_e32 v130, v144, v99
	v_mfma_f32_16x16x32_bf16 v[112:115], v[148:151], v[42:45], v[54:57]
	v_add_u32_e32 v140, v144, v100
	v_add_u32_e32 v145, v144, v101
	s_nop 0
	v_mul_f32_e32 v54, 0x41800000, v160
	s_waitcnt lgkmcnt(0)
	v_mfma_f32_16x16x32_bf16 v[42:45], v[156:159], v[42:45], v[46:49]
	s_add_i32 s37, s77, s70
	s_xor_b32 s79, s79, 1
	s_min_i32 s37, s37, s71
	s_mul_i32 s58, s79, 0x12000
	s_add_i32 s37, s37, s3
	v_add_u32_e32 v2, s58, v84
	s_mul_hi_i32 s58, s37, 0x2aaaaaab
	s_lshr_b32 s59, s58, 31
	s_ashr_i32 s58, s58, 4
	s_add_i32 s59, s58, s59
	s_mul_i32 s58, s59, 0x60
	s_sub_i32 s37, s37, s58
	s_ashr_i32 s58, s59, 3
	s_and_b32 s80, s59, 7
	v_add_u32_e32 v3, v2, v83
	s_cmp_gt_i32 s37, 31
	ds_write_b128 v3, v[38:41]
	ds_write_b128 v3, v[34:37] offset:36864
	v_add_u32_e32 v3, v2, v85
	s_cselect_b64 s[82:83], -1, 0
	s_cmp_gt_i32 s37, 63
	ds_write_b128 v3, v[30:33]
	ds_write_b128 v3, v[26:29] offset:36864
	v_add_u32_e32 v3, v2, v87
	v_add_u32_e32 v2, v2, v88
	s_cselect_b64 s[86:87], -1, 0
	ds_write_b128 v3, v[22:25]
	ds_write_b128 v3, v[18:21] offset:36864
	ds_write_b128 v2, v[14:17]
	ds_write_b128 v2, v[10:13] offset:36864
	v_cndmask_b32_e64 v2, 0, 1, s[86:87]
	s_cmp_lg_u64 s[82:83], 0
	v_readfirstlane_b32 s59, v2
	s_addc_u32 s81, s59, 0
	s_lshl_b32 s59, s81, 5
	s_lshl_b32 s82, s81, 1
	s_sub_i32 s37, s37, s59
	s_sub_i32 s59, 5, s82
	s_ashr_i32 s83, s37, s59
	s_lshl_b32 s59, -1, s59
	s_andn2_b32 s84, s37, s59
	s_ashr_i32 s59, s58, 31
	s_lshl_b64 s[86:87], s[58:59], 12
	s_ashr_i32 s37, s83, 31
	s_add_u32 s59, s86, s83
	s_addc_u32 s37, s87, s37
	s_mulk_i32 s37, 0xa00
	s_mul_hi_u32 s86, s59, 0xa00
	s_add_i32 s87, s86, s37
	s_mulk_i32 s59, 0xa00
	s_lshl_b32 s37, s80, 6
	s_or_b32 s86, s59, s37
	s_lshl_b64 s[86:87], s[86:87], 1
	s_add_u32 s37, s33, s86
	s_addc_u32 s59, s66, s87
	s_add_u32 s86, s37, 0x400
	s_addc_u32 s87, s59, 0
	s_lshl_b32 s59, s84, 7
	v_add_u32_e32 v2, s59, v81
	s_lshl_b32 s37, 0x1400, s82
	v_max_i32_e32 v3, 0, v2
	v_mul_u32_u24_e32 v3, s37, v3
	v_or_b32_e32 v3, v3, v80
	global_load_dwordx4 v[38:41], v3, s[86:87]
	global_load_dwordx4 v[34:37], v3, s[86:87] offset:1024
	v_max_i32_e32 v3, 0xffffffc0, v2
	v_add_u32_e32 v3, 64, v3
	v_mul_u32_u24_e32 v3, s37, v3
	v_or_b32_e32 v3, v3, v80
	global_load_dwordx4 v[30:33], v3, s[86:87]
	global_load_dwordx4 v[26:29], v3, s[86:87] offset:1024
	v_add_u32_e32 v3, s59, v1
	v_max_i32_e32 v2, 0xffffff40, v2
	v_max_i32_e32 v3, 0, v3
	v_add_u32_e32 v2, 0xc0, v2
	v_mul_u32_u24_e32 v3, s37, v3
	v_mul_u32_u24_e32 v2, s37, v2
	v_or_b32_e32 v3, v3, v80
	v_or_b32_e32 v2, v2, v80
	s_ashr_i32 s37, s36, 31
	global_load_dwordx4 v[22:25], v3, s[86:87]
	global_load_dwordx4 v[18:21], v3, s[86:87] offset:1024
	global_load_dwordx4 v[14:17], v2, s[86:87]
	global_load_dwordx4 v[10:13], v2, s[86:87] offset:1024
	s_lshl_b64 s[86:87], s[36:37], 12
	s_ashr_i32 s37, s73, 31
	s_add_u32 s59, s86, s73
	s_addc_u32 s37, s87, s37
	s_mulk_i32 s37, 0xa00
	s_mul_hi_u32 s86, s59, 0xa00
	s_add_i32 s87, s86, s37
	s_mulk_i32 s59, 0xa00
	s_lshl_b32 s37, s75, 6
	s_or_b32 s86, s59, s37
	s_lshl_b64 s[86:87], s[86:87], 1
	s_add_u32 s86, s33, s86
	s_addc_u32 s87, s66, s87
	s_lshl_b32 s37, 0x1400, s74
	v_lshl_add_u32 v2, s76, 7, v86
	s_and_b32 s37, s37, 0x555400
	v_mul_u32_u24_e32 v2, s37, v2
	v_or_b32_e32 v6, v2, v82
	global_load_dwordx4 v[2:5], v6, s[86:87]
	s_nop 0
	global_load_dwordx4 v[6:9], v6, s[86:87] offset:64
	v_cndmask_b32_e32 v54, v109, v54, vcc
	s_or_b64 vcc, s[64:65], s[54:55]
	v_pk_fma_f32 v[56:57], v[50:51], v[160:161], v[54:55] op_sel_hi:[1,0,0]
	v_mul_f32_e32 v46, 0, v160
	v_cndmask_b32_e32 v46, v109, v46, vcc
	v_pk_fma_f32 v[48:49], v[50:51], v[160:161], v[46:47] op_sel_hi:[1,0,0]
	v_pk_fma_f32 v[46:47], v[52:53], v[160:161], v[46:47] op_sel_hi:[1,0,0]
	v_pk_fma_f32 v[54:55], v[52:53], v[160:161], v[54:55] op_sel_hi:[1,0,0]
	v_pk_fma_f32 v[44:45], v[44:45], s[56:57], v[46:47] op_sel_hi:[1,0,1]
	v_pk_fma_f32 v[42:43], v[42:43], s[56:57], v[48:49] op_sel_hi:[1,0,1]
	v_cndmask_b32_e64 v48, v109, v44, s[18:19]
	v_and_b32_e32 v44, 64, v108
	v_pk_fma_f32 v[54:55], v[114:115], s[56:57], v[54:55] op_sel_hi:[1,0,1]
	v_cndmask_b32_e64 v47, v109, v43, s[16:17]
	v_cndmask_b32_e64 v49, v109, v45, s[20:21]
	v_xor_b32_e32 v43, 16, v108
	v_add_u32_e32 v44, 64, v44
	v_pk_fma_f32 v[56:57], v[112:113], s[56:57], v[56:57] op_sel_hi:[1,0,1]
	v_max_f32_e32 v112, v54, v55
	v_cndmask_b32_e64 v46, v109, v42, s[14:15]
	v_max_f32_e32 v42, v48, v49
	v_cmp_lt_i32_e32 vcc, v43, v44
	v_max3_f32 v112, v56, v57, v112
	v_max3_f32 v42, v46, v47, v42
	v_cndmask_b32_e32 v43, v108, v43, vcc
	v_max3_f32 v42, v111, v112, v42
	v_lshlrev_b32_e32 v142, 2, v43
	v_mov_b32_e32 v168, v42
	s_nop 1
	v_permlane16_swap_b32_e32 v168, v42
	v_max_f32_e32 v42, v42, v168
	v_xor_b32_e32 v43, 32, v108
	v_cmp_lt_i32_e32 vcc, v43, v44
	s_nop 1
	v_cndmask_b32_e32 v43, v108, v43, vcc
	v_lshlrev_b32_e32 v143, 2, v43
	v_mov_b32_e32 v168, v42
	s_nop 1
	v_permlane32_swap_b32_e32 v168, v42
	v_max_f32_e32 v111, v42, v168
	v_xor_b32_e32 v42, 0x80000000, v111
	v_mov_b32_e32 v43, v42
	v_mov_b32_e32 v44, v42
	v_mov_b32_e32 v45, v42
	ds_read_b64_tr_b16 v[120:121], v130 offset:36864
	v_pk_add_f32 v[118:119], v[166:167], v[44:45]
	v_pk_add_f32 v[112:113], v[164:165], v[44:45]
	v_exp_f32_e32 v126, v118
	v_exp_f32_e32 v127, v119
	ds_read_b64_tr_b16 v[118:119], v130 offset:36872
	v_pk_add_f32 v[114:115], v[162:163], v[42:43]
	v_exp_f32_e32 v112, v112
	v_exp_f32_e32 v114, v114
	v_exp_f32_e32 v113, v113
	v_exp_f32_e32 v115, v115
	ds_read_b64_tr_b16 v[128:129], v130 offset:36928
	ds_read_b64_tr_b16 v[130:131], v130 offset:36936
	v_pk_add_f32 v[134:135], v[76:77], v[42:43]
	v_cvt_pk_bf16_f32 v123, v112, v113
	v_cvt_pk_bf16_f32 v122, v114, v115
	v_pk_add_f32 v[116:117], v[112:113], 0 op_sel_hi:[1,0]
	v_pk_add_f32 v[124:125], v[114:115], 0 op_sel_hi:[1,0]
	s_waitcnt lgkmcnt(3)
; #define LAS __attribute__((address_space(3)))
; __device__ __forceinline__ unsigned cvt_pk_bf16(float lo, float hi) { const f32x2_t v = {lo, hi}; return __builtin_bit_cast(unsigned, __builtin_convertvector(v, bf16x2_t)); }
; __device__ __forceinline__ float fast_exp2(float x) { return __builtin_amdgcn_exp2f(x); }
; __device__ __forceinline__ s16x4 tr_read(LAS unsigned char* p) { return __builtin_bit_cast(s16x4, __builtin_amdgcn_ds_read_tr16_b64_v4i16((LAS s16x4*)p)); }
; __device__ __forceinline__ void phase_attn(Frame& F) {
;     ...
;         for (int T = 0; T < 9; ++T) { const f32x4 d = St[T] + nmx; f32x4 pv; pv.x = fast_exp2(d.x); pv.y = fast_exp2(d.y); pv.z = fast_exp2(d.z); pv.w = fast_exp2(d.w); St[T] = pv; lv = lv + pv; }
;         float l = (lv.x + lv.y) + (lv.z + lv.w);
;         l += __shfl_xor(l, 16); l += __shfl_xor(l, 32);
;         f32x4 O[4];
; #pragma unroll
;         for (int dt = 0; dt < 4; ++dt) O[dt] = (f32x4){0.f, 0.f, 0.f, 0.f};
; #pragma unroll
;         for (int T = 0; T < 9; ++T) {
;             u32x2 pw; pw.x = cvt_pk_bf16(St[T][0], St[T][1]); pw.y = cvt_pk_bf16(St[T][2], St[T][3]);
;             const s16x4 pb = __builtin_bit_cast(s16x4, pw);
;             LAS unsigned char* va = kb + ATT_VOFF + (16 * (w + T) + 4 * fq + (fr >> 2)) * ATT_ROWB + (8 * (fr & 3)) * 2;
; #pragma unroll
;             for (int dt = 0; dt < 4; ++dt) O[dt] = __builtin_amdgcn_mfma_f32_16x16x16bf16_1k(tr_read(va + 64 * (dt >> 1) + 8 * (dt & 1)), pb, O[dt], 0, 0, 0);
;         }
	v_mfma_f32_16x16x16_bf16 v[112:115], v[120:121], v[122:123], 0
	v_add_f32_e64 v120, v74, v44
	v_add_f32_e64 v121, v75, v45
	v_pk_add_f32 v[132:133], v[126:127], v[116:117]
	v_exp_f32_e32 v136, v120
	s_waitcnt lgkmcnt(2)
	v_mfma_f32_16x16x16_bf16 v[116:119], v[118:119], v[122:123], 0
	v_exp_f32_e32 v137, v121
	v_pk_add_f32 v[78:79], v[78:79], v[42:43]
	v_cvt_pk_bf16_f32 v139, v126, v127
	s_waitcnt lgkmcnt(1)
	v_mfma_f32_16x16x16_bf16 v[74:77], v[128:129], v[122:123], 0
	ds_read_b64_tr_b16 v[128:129], v140 offset:36864
	v_exp_f32_e32 v78, v78
	v_exp_f32_e32 v79, v79
	s_waitcnt lgkmcnt(1)
	v_mfma_f32_16x16x16_bf16 v[120:123], v[130:131], v[122:123], 0
	ds_read_b64_tr_b16 v[130:131], v140 offset:36872
	ds_read_b64_tr_b16 v[126:127], v140 offset:36928
	ds_read_b64_tr_b16 v[140:141], v140 offset:36936
	v_cvt_pk_bf16_f32 v138, v78, v79
	v_exp_f32_e32 v134, v134
	v_exp_f32_e32 v135, v135
	s_waitcnt lgkmcnt(3)
	v_mfma_f32_16x16x16_bf16 v[112:115], v[128:129], v[138:139], v[112:115]
	v_add_f32_e64 v128, v70, v44
	v_add_f32_e64 v129, v71, v45
	v_pk_add_f32 v[78:79], v[78:79], v[124:125]
	v_pk_add_f32 v[124:125], v[136:137], v[132:133]
	s_waitcnt lgkmcnt(2)
	v_mfma_f32_16x16x16_bf16 v[116:119], v[130:131], v[138:139], v[116:119]
	v_add_f32_e64 v130, v72, v42
	v_add_f32_e64 v131, v73, v43
	v_pk_add_f32 v[78:79], v[134:135], v[78:79]
	v_exp_f32_e32 v128, v128
	s_waitcnt lgkmcnt(1)
	v_mfma_f32_16x16x16_bf16 v[70:73], v[126:127], v[138:139], v[74:77]
	ds_read_b64_tr_b16 v[126:127], v145 offset:36864
	v_exp_f32_e32 v129, v129
	v_pk_add_f32 v[48:49], v[44:45], v[48:49]
	s_waitcnt lgkmcnt(1)
	v_mfma_f32_16x16x16_bf16 v[74:77], v[140:141], v[138:139], v[120:123]
	v_add_f32_e64 v124, v128, v124
	v_add_f32_e64 v125, v129, v125
	s_nop 0
	ds_read_b64_tr_b16 v[120:121], v145 offset:36872
	v_cvt_pk_bf16_f32 v122, v134, v135
	ds_read_b64_tr_b16 v[132:133], v145 offset:36928
	ds_read_b64_tr_b16 v[134:135], v145 offset:36936
	v_cvt_pk_bf16_f32 v123, v136, v137
	v_add_u32_e32 v136, v144, v102
	s_waitcnt lgkmcnt(3)
	v_mfma_f32_16x16x16_bf16 v[112:115], v[126:127], v[122:123], v[112:115]
	v_exp_f32_e32 v126, v130
	v_exp_f32_e32 v127, v131
	v_pk_add_f32 v[130:131], v[68:69], v[42:43]
	s_waitcnt lgkmcnt(2)
	v_mfma_f32_16x16x16_bf16 v[116:119], v[120:121], v[122:123], v[116:119]
	v_add_f32_e64 v120, v66, v44
	v_add_f32_e64 v121, v67, v45
	v_pk_add_f32 v[78:79], v[126:127], v[78:79]
	v_exp_f32_e32 v130, v130
	s_waitcnt lgkmcnt(1)
	v_mfma_f32_16x16x16_bf16 v[66:69], v[132:133], v[122:123], v[70:73]
	ds_read_b64_tr_b16 v[132:133], v136 offset:36864
	v_exp_f32_e32 v120, v120
	v_exp_f32_e32 v121, v121
	s_waitcnt lgkmcnt(1)
	v_mfma_f32_16x16x16_bf16 v[70:73], v[134:135], v[122:123], v[74:77]
	ds_read_b64_tr_b16 v[122:123], v136 offset:36872
	v_cvt_pk_bf16_f32 v134, v126, v127
	v_cvt_pk_bf16_f32 v135, v128, v129
	ds_read_b64_tr_b16 v[128:129], v136 offset:36928
	ds_read_b64_tr_b16 v[136:137], v136 offset:36936
	s_waitcnt lgkmcnt(3)
	v_mfma_f32_16x16x16_bf16 v[74:77], v[132:133], v[134:135], v[112:115]
	v_add_u32_e32 v132, v144, v103
	ds_read_b64_tr_b16 v[126:127], v132 offset:36872
	v_exp_f32_e32 v131, v131
	s_waitcnt lgkmcnt(3)
	v_mfma_f32_16x16x16_bf16 v[112:115], v[122:123], v[134:135], v[116:119]
	ds_read_b64_tr_b16 v[122:123], v132 offset:36864
	v_pk_add_f32 v[124:125], v[120:121], v[124:125]
	v_pk_add_f32 v[78:79], v[130:131], v[78:79]
	v_pk_add_f32 v[116:117], v[62:63], v[44:45]
	v_pk_add_f32 v[118:119], v[64:65], v[42:43]
	s_waitcnt lgkmcnt(3)
	v_mfma_f32_16x16x16_bf16 v[62:65], v[128:129], v[134:135], v[66:69]
	v_exp_f32_e32 v116, v116
	v_exp_f32_e32 v117, v117
	v_cvt_pk_bf16_f32 v128, v130, v131
	v_cvt_pk_bf16_f32 v129, v120, v121
	ds_read_b64_tr_b16 v[120:121], v132 offset:36928
	ds_read_b64_tr_b16 v[130:131], v132 offset:36936
	v_add_u32_e32 v132, v144, v104
	s_waitcnt lgkmcnt(4)
	v_mfma_f32_16x16x16_bf16 v[66:69], v[136:137], v[134:135], v[70:73]
	v_exp_f32_e32 v118, v118
	v_exp_f32_e32 v119, v119
	s_waitcnt lgkmcnt(2)
	v_mfma_f32_16x16x16_bf16 v[70:73], v[122:123], v[128:129], v[74:77]
	v_add_f32_e64 v122, v116, v124
	v_add_f32_e64 v123, v117, v125
	ds_read_b64_tr_b16 v[124:125], v132 offset:36872
	v_pk_add_f32 v[78:79], v[118:119], v[78:79]
	v_mfma_f32_16x16x16_bf16 v[74:77], v[126:127], v[128:129], v[112:115]
	v_cvt_pk_bf16_f32 v127, v116, v117
	v_cvt_pk_bf16_f32 v126, v118, v119
	s_nop 0
	v_pk_add_f32 v[112:113], v[58:59], v[44:45]
	v_pk_add_f32 v[114:115], v[60:61], v[42:43]
	s_waitcnt lgkmcnt(2)
	v_mfma_f32_16x16x16_bf16 v[58:61], v[120:121], v[128:129], v[62:65]
	ds_read_b64_tr_b16 v[120:121], v132 offset:36864
	v_exp_f32_e32 v112, v112
	v_exp_f32_e32 v113, v113
	v_exp_f32_e32 v114, v114
	s_waitcnt lgkmcnt(2)
	v_mfma_f32_16x16x16_bf16 v[62:65], v[130:131], v[128:129], v[66:69]
	ds_read_b64_tr_b16 v[116:117], v132 offset:36928
	ds_read_b64_tr_b16 v[128:129], v132 offset:36936
	v_exp_f32_e32 v115, v115
	v_pk_add_f32 v[118:119], v[112:113], v[122:123]
	v_add_u32_e32 v122, v144, v105
	s_waitcnt lgkmcnt(2)
; #define LAS __attribute__((address_space(3)))
; __device__ __forceinline__ unsigned cvt_pk_bf16(float lo, float hi) { const f32x2_t v = {lo, hi}; return __builtin_bit_cast(unsigned, __builtin_convertvector(v, bf16x2_t)); }
; __device__ __forceinline__ s16x4 tr_read(LAS unsigned char* p) { return __builtin_bit_cast(s16x4, __builtin_amdgcn_ds_read_tr16_b64_v4i16((LAS s16x4*)p)); }
; __device__ __forceinline__ void phase_attn(Frame& F) {
;     ...
;         for (int T = 0; T < 9; ++T) {
;             u32x2 pw; pw.x = cvt_pk_bf16(St[T][0], St[T][1]); pw.y = cvt_pk_bf16(St[T][2], St[T][3]);
;             const s16x4 pb = __builtin_bit_cast(s16x4, pw);
;             LAS unsigned char* va = kb + ATT_VOFF + (16 * (w + T) + 4 * fq + (fr >> 2)) * ATT_ROWB + (8 * (fr & 3)) * 2;
; #pragma unroll
;             for (int dt = 0; dt < 4; ++dt) O[dt] = __builtin_amdgcn_mfma_f32_16x16x16bf16_1k(tr_read(va + 64 * (dt >> 1) + 8 * (dt & 1)), pb, O[dt], 0, 0, 0);
;         }
;         const float inv = 1.f / l;
;         bf16_t* op = (bf16_t*)((char*)part + (((size_t)cu.dsel * NTOK + (size_t)cu.b * SEQ + cu.r) * 512 + cu.h * 64) * 2 + (qrow * 1024u + 16u * fq));
; #pragma unroll
;         for (int u2 = 0; u2 < 2; ++u2) { u32x4 o4; o4.x = cvt_pk_bf16(O[2 * u2][0] * inv, O[2 * u2][1] * inv); o4.y = cvt_pk_bf16(O[2 * u2][2] * inv, O[2 * u2][3] * inv);
;             o4.z = cvt_pk_bf16(O[2 * u2 + 1][0] * inv, O[2 * u2 + 1][1] * inv); o4.w = cvt_pk_bf16(O[2 * u2 + 1][2] * inv, O[2 * u2 + 1][3] * inv); *(u32x4*)(op + 32 * u2) = o4; }
;         if (fq == 0) *(float*)((char*)lse + (((size_t)cu.dsel * NTOK + (size_t)cu.b * SEQ + cu.r) * 8 + cu.h) * 4 + qrow * 32u) = mx + __builtin_amdgcn_logf(l);
;         cu = nu; buf ^= 1;
	v_mfma_f32_16x16x16_bf16 v[66:69], v[120:121], v[126:127], v[70:73]
	ds_read_b64_tr_b16 v[120:121], v122 offset:36872
	v_mfma_f32_16x16x16_bf16 v[70:73], v[124:125], v[126:127], v[74:77]
	s_nop 2
	v_add_f32_e64 v74, v114, v78
	v_add_f32_e64 v75, v115, v79
	v_pk_add_f32 v[76:77], v[54:55], v[44:45]
	v_pk_add_f32 v[78:79], v[56:57], v[42:43]
	s_waitcnt lgkmcnt(2)
	v_mfma_f32_16x16x16_bf16 v[54:57], v[116:117], v[126:127], v[58:61]
	ds_read_b64_tr_b16 v[116:117], v122 offset:36864
	v_cvt_pk_bf16_f32 v114, v114, v115
	v_cvt_pk_bf16_f32 v115, v112, v113
	ds_read_b64_tr_b16 v[112:113], v122 offset:36928
	ds_read_b64_tr_b16 v[122:123], v122 offset:36936
	s_waitcnt lgkmcnt(4)
	v_mfma_f32_16x16x16_bf16 v[58:61], v[128:129], v[126:127], v[62:65]
	v_exp_f32_e32 v76, v76
	v_exp_f32_e32 v77, v77
	v_exp_f32_e32 v78, v78
	s_waitcnt lgkmcnt(2)
	v_mfma_f32_16x16x16_bf16 v[62:65], v[116:117], v[114:115], v[66:69]
	v_exp_f32_e32 v79, v79
	v_pk_add_f32 v[116:117], v[76:77], v[118:119]
	v_mfma_f32_16x16x16_bf16 v[66:69], v[120:121], v[114:115], v[70:73]
	s_nop 2
	v_add_f32_e64 v70, v42, v46
	v_add_f32_e64 v71, v43, v47
	s_waitcnt lgkmcnt(1)
	v_mfma_f32_16x16x16_bf16 v[42:45], v[112:113], v[114:115], v[54:57]
	v_exp_f32_e32 v72, v48
	v_exp_f32_e32 v73, v49
	v_exp_f32_e32 v70, v70
	v_add_u32_e32 v56, v144, v106
	ds_read_b64_tr_b16 v[54:55], v56 offset:36864
	s_waitcnt lgkmcnt(1)
	v_mfma_f32_16x16x16_bf16 v[46:49], v[122:123], v[114:115], v[58:61]
	v_exp_f32_e32 v71, v71
	v_cvt_pk_bf16_f32 v112, v78, v79
	v_cvt_pk_bf16_f32 v113, v76, v77
	ds_read_b64_tr_b16 v[58:59], v56 offset:36872
	ds_read_b64_tr_b16 v[76:77], v56 offset:36928
	ds_read_b64_tr_b16 v[114:115], v56 offset:36936
	s_waitcnt lgkmcnt(3)
	v_mfma_f32_16x16x16_bf16 v[54:57], v[54:55], v[112:113], v[62:65]
	s_nop 2
	v_add_f32_e64 v62, v78, v74
	v_add_f32_e64 v63, v79, v75
	v_pk_add_f32 v[64:65], v[72:73], v[116:117]
	v_pk_add_f32 v[62:63], v[70:71], v[62:63]
	v_add_u32_e32 v74, v144, v107
	s_waitcnt lgkmcnt(2)
	v_mfma_f32_16x16x16_bf16 v[58:61], v[58:59], v[112:113], v[66:69]
	s_nop 2
	v_pk_mov_b32 v[66:67], v[62:63], v[64:65] op_sel:[1,0]
	v_mov_b32_e32 v63, v65
	ds_read_b64_tr_b16 v[64:65], v74 offset:36864
	v_pk_add_f32 v[62:63], v[66:67], v[62:63]
	v_cvt_pk_bf16_f32 v66, v70, v71
	v_add_f32_e32 v75, v62, v63
	v_cvt_pk_bf16_f32 v67, v72, v73
	s_waitcnt lgkmcnt(2)
	v_mfma_f32_16x16x16_bf16 v[42:45], v[76:77], v[112:113], v[42:45]
	ds_read_b64_tr_b16 v[62:63], v74 offset:36872
	ds_read_b64_tr_b16 v[68:69], v74 offset:36928
	ds_read_b64_tr_b16 v[70:71], v74 offset:36936
	s_waitcnt lgkmcnt(3)
	v_mfma_f32_16x16x16_bf16 v[54:57], v[64:65], v[66:67], v[54:57]
	v_mov_b32_e32 v168, v75
	s_waitcnt lgkmcnt(0)
	s_nop 0
	v_permlane16_swap_b32_e32 v168, v75
	v_add_f32_e32 v72, v75, v168
	v_mov_b32_e32 v169, v72
	v_mfma_f32_16x16x16_bf16 v[58:61], v[62:63], v[66:67], v[58:61]
	v_mfma_f32_16x16x16_bf16 v[62:65], v[68:69], v[66:67], v[42:45]
	v_permlane32_swap_b32_e32 v169, v72
	s_nop 1
	v_add_f32_e32 v43, v72, v169
	v_div_scale_f32 v68, s[64:65], v43, v43, 1.0
	v_mfma_f32_16x16x16_bf16 v[46:49], v[114:115], v[112:113], v[46:49]
	v_rcp_f32_e32 v69, v68
	v_lshlrev_b32_e32 v42, s35, v110
	s_ashr_i32 s35, s34, 31
	v_mfma_f32_16x16x16_bf16 v[44:47], v[70:71], v[66:67], v[46:49]
	s_lshl_b64 s[64:65], s[26:27], 16
	s_lshl_b64 s[34:35], s[34:35], 12
	s_ashr_i32 s26, s31, 31
	s_nop 0
	v_fma_f32 v48, -v68, v69, 1.0
	v_fmac_f32_e32 v69, v48, v69
	v_div_scale_f32 v48, vcc, 1.0, v43, 1.0
	v_mul_f32_e32 v49, v48, v69
	s_add_u32 s31, s34, s31
	v_fma_f32 v66, -v68, v49, v48
	s_addc_u32 s26, s35, s26
	v_fmac_f32_e32 v49, v66, v69
	s_add_u32 s34, s31, s64
	v_fma_f32 v48, -v68, v49, v48
	s_addc_u32 s35, s26, s65
	v_div_fmas_f32 v48, v48, v69, v49
	s_lshl_b32 s26, s30, 7
	s_lshl_b64 s[64:65], s[34:35], 10
	v_div_fixup_f32 v48, v48, v43, 1.0
	s_add_u32 s31, s24, s64
	v_lshl_or_b32 v49, v42, 10, v82
	s_addc_u32 s37, s25, s65
	v_pk_mul_f32 v[54:55], v[48:49], v[54:55] op_sel_hi:[0,1]
	v_pk_mul_f32 v[56:57], v[48:49], v[56:57] op_sel_hi:[0,1]
	s_add_u32 s64, s31, s26
	v_cvt_pk_bf16_f32 v54, v54, v55
	v_cvt_pk_bf16_f32 v55, v56, v57
	v_pk_mul_f32 v[56:57], v[48:49], v[58:59] op_sel_hi:[0,1]
	v_pk_mul_f32 v[58:59], v[48:49], v[60:61] op_sel_hi:[0,1]
	s_addc_u32 s65, s37, 0
	v_cvt_pk_bf16_f32 v56, v56, v57
	v_cvt_pk_bf16_f32 v57, v58, v59
	global_store_dwordx4 v49, v[54:57], s[64:65]
	v_pk_mul_f32 v[44:45], v[48:49], v[44:45] op_sel_hi:[0,1]
	s_nop 0
	v_pk_mul_f32 v[54:55], v[48:49], v[62:63] op_sel_hi:[0,1]
	v_pk_mul_f32 v[56:57], v[48:49], v[64:65] op_sel_hi:[0,1]
	v_cvt_pk_bf16_f32 v54, v54, v55
	v_cvt_pk_bf16_f32 v55, v56, v57
	v_cvt_pk_bf16_f32 v56, v44, v45
	v_pk_mul_f32 v[44:45], v[48:49], v[46:47] op_sel_hi:[0,1]
	v_cvt_pk_bf16_f32 v57, v44, v45
	global_store_dwordx4 v49, v[54:57], s[64:65] offset:64
	s_and_saveexec_b64 s[64:65], s[4:5]
	s_cbranch_execz .LBB0_303
	s_mov_b32 s31, s27
	v_log_f32_e32 v43, v43
	s_lshl_b64 s[34:35], s[34:35], 5
	s_lshl_b64 s[30:31], s[30:31], 2
	s_add_u32 s26, s67, s34
	s_addc_u32 s34, s68, s35
	s_add_u32 s30, s26, s30
	v_add_f32_e32 v43, v111, v43
	s_addc_u32 s31, s34, s31
	v_lshlrev_b32_e32 v42, 5, v42
	global_store_dword v42, v43, s[30:31]
	s_branch .LBB0_303

; #define PG8_STAGE(bufoff, gbase, voff) do { _Pragma("unroll") for (int _i = 0; _i < 2; ++_i) \
;         __builtin_amdgcn_global_load_lds((const unsigned*)((const char*)(gbase) + (voff)[_i]), (LAS unsigned*)(lds + (bufoff) + ldsw + _i * 8192), 16, 0, 0); } while (0)
; #define PG8_LDA(dst, b, h) do { _Pragma("unroll") for (int m = 0; m < 4; ++m) _Pragma("unroll") for (int k = 0; k < 2; ++k) dst[m][k] = *(const LAS bf16x8*)(lds + PG8_SA(b, h) + aoff + m * 2048 + k * 1024); } while (0)
; #define PG8_LDB(dst, b, h) do { _Pragma("unroll") for (int n = 0; n < 2; ++n) _Pragma("unroll") for (int k = 0; k < 2; ++k) dst[n][k] = *(const LAS bf16x8*)(lds + PG8_SB(b, h) + boff + n * 2048 + k * 1024); } while (0)
; #define PG8_WAIT_V(n) asm volatile("s_waitcnt vmcnt(" #n ")" ::: "memory")
; #define PG8_WAIT_L(n) asm volatile("s_waitcnt lgkmcnt(" #n ")" ::: "memory")
; #define PG8_BAR __builtin_amdgcn_s_barrier()
; #define PG8_SCHED __builtin_amdgcn_sched_barrier(0)
;     ...
;             const bool last = (t == nt - 2);
;             const char* a1 = cA + (size_t)(t + 1) * kstep;
;             const char* a2 = last ? nA : cA + (size_t)(t + 2) * kstep; const char* b2 = last ? nB : cB + (size_t)(t + 2) * kstep;
;             const char* a3 = a2 + kstep; const char* b3 = b2 + kstep;
;             unsigned v2[2][2];
;             if constexpr (GATHER) { v2[0][0] = last ? vn[0][0] : va[0][0]; v2[0][1] = last ? vn[0][1] : va[0][1]; v2[1][0] = last ? vn[1][0] : va[1][0]; v2[1][1] = last ? vn[1][1] : va[1][1]; }
;             else { v2[0][0] = va[0][0]; v2[0][1] = va[0][1]; v2[1][0] = va[0][0]; v2[1][1] = va[0][1]; }
;             if constexpr (SP2) {
;             PG8_LDB(B0, 0, 0); PG8_LDB(B1, 0, 1); PG8_SCHED; PG8_LDA(At, 0, 0); PG8_STAGE(PG8_SA(1, 1), a1 + ah, VA1);
;             PG8_WAIT_V(8); PG8_WAIT_L(0); PG8_BAR; PG8_MMA(0, 0, At, B0); PG8_MMA(0, 1, At, B1); PG8_BAR; PG8_SCHED;
;             PG8_LDA(At, 0, 1); PG8_STAGE(PG8_SB(0, 0), b2, voffB); PG8_STAGE(PG8_SB(0, 1), b2 + bstep, voffB); PG8_STAGE(PG8_SA(0, 0), a2, v2[0]);
;             PG8_WAIT_V(8); PG8_WAIT_L(0); PG8_BAR; if (full) { PG8_MMA(1, 0, At, B0); PG8_MMA(1, 1, At, B1); } PG8_BAR; PG8_SCHED;
.LBB0_735:
	ds_read_b128 v[26:29], v232
	ds_read_b128 v[30:33], v232 offset:1024
	ds_read_b128 v[18:21], v232 offset:2048
	ds_read_b128 v[22:25], v232 offset:3072
	ds_read_b128 v[10:13], v233
	ds_read_b128 v[14:17], v233 offset:1024
	ds_read_b128 v[2:5], v233 offset:2048
	ds_read_b128 v[6:9], v233 offset:3072
	s_add_u32 s4, s24, s28
	s_addc_u32 s5, s25, s29
	s_add_u32 s30, s4, 0x319d0100
	s_addc_u32 s31, s5, 0
	s_add_u32 s75, s72, s28
	s_addc_u32 s76, s73, s29
	s_cmpk_eq_i32 s28, 0x300
	s_cselect_b64 s[4:5], -1, 0
	s_and_b64 s[6:7], s[4:5], exec
	v_cndmask_b32_e64 v66, v240, v236, s[4:5]
	s_cselect_b32 s35, s9, s31
	s_cselect_b32 s34, s8, s30
	v_cndmask_b32_e64 v68, v206, v237, s[4:5]
	s_cselect_b32 s31, s21, s76
	s_cselect_b32 s30, s71, s75
	s_mov_b32 m0, s53
	v_lshl_add_u64 v[212:213], v[210:211], 0, s[28:29]
	ds_read_b128 v[34:37], v234
	ds_read_b128 v[38:41], v234 offset:1024
	ds_read_b128 v[42:45], v234 offset:2048
	ds_read_b128 v[46:49], v234 offset:3072
	ds_read_b128 v[50:53], v234 offset:4096
	ds_read_b128 v[54:57], v234 offset:5120
	ds_read_b128 v[58:61], v234 offset:6144
	ds_read_b128 v[62:65], v234 offset:7168
	global_load_lds_dwordx4 v[212:213], off
	v_lshl_add_u64 v[212:213], v[208:209], 0, s[28:29]
	s_mov_b32 m0, s54
	s_nop 0
	global_load_lds_dwordx4 v[212:213], off
	s_waitcnt vmcnt(8)
	s_waitcnt lgkmcnt(0)
	s_barrier
	s_setprio 1
	s_waitcnt lgkmcnt(0)
	v_mfma_scale_f32_16x16x128_f8f6f4 v[186:189], v[26:33], v[34:41], v[186:189], v216, v217 op_sel_hi:[0,0,0]
	v_mfma_scale_f32_16x16x128_f8f6f4 v[194:197], v[18:25], v[34:41], v[194:197], v216, v217 op_sel_hi:[0,0,0]
	v_mfma_scale_f32_16x16x128_f8f6f4 v[170:173], v[26:33], v[42:49], v[170:173], v216, v217 op_sel_hi:[0,0,0]
	v_mfma_scale_f32_16x16x128_f8f6f4 v[178:181], v[18:25], v[42:49], v[178:181], v216, v217 op_sel_hi:[0,0,0]
	v_mfma_scale_f32_16x16x128_f8f6f4 v[154:157], v[26:33], v[50:57], v[154:157], v216, v217 op_sel_hi:[0,0,0]
	v_mfma_scale_f32_16x16x128_f8f6f4 v[162:165], v[18:25], v[50:57], v[162:165], v216, v217 op_sel_hi:[0,0,0]
	v_mfma_scale_f32_16x16x128_f8f6f4 v[142:145], v[26:33], v[58:65], v[142:145], v216, v217 op_sel_hi:[0,0,0]
	v_mfma_scale_f32_16x16x128_f8f6f4 v[146:149], v[18:25], v[58:65], v[146:149], v216, v217 op_sel_hi:[0,0,0]
	s_setprio 0
	s_setprio 1
	v_mfma_scale_f32_16x16x128_f8f6f4 v[182:185], v[10:17], v[34:41], v[182:185], v216, v217 op_sel_hi:[0,0,0]
	v_mfma_scale_f32_16x16x128_f8f6f4 v[190:193], v[2:9], v[34:41], v[190:193], v216, v217 op_sel_hi:[0,0,0]
	v_mfma_scale_f32_16x16x128_f8f6f4 v[166:169], v[10:17], v[42:49], v[166:169], v216, v217 op_sel_hi:[0,0,0]
	v_mfma_scale_f32_16x16x128_f8f6f4 v[174:177], v[2:9], v[42:49], v[174:177], v216, v217 op_sel_hi:[0,0,0]
	v_mfma_scale_f32_16x16x128_f8f6f4 v[150:153], v[10:17], v[50:57], v[150:153], v216, v217 op_sel_hi:[0,0,0]
	v_mfma_scale_f32_16x16x128_f8f6f4 v[158:161], v[2:9], v[50:57], v[158:161], v216, v217 op_sel_hi:[0,0,0]
	v_mfma_scale_f32_16x16x128_f8f6f4 v[134:137], v[10:17], v[58:65], v[134:137], v216, v217 op_sel_hi:[0,0,0]
	v_mfma_scale_f32_16x16x128_f8f6f4 v[138:141], v[2:9], v[58:65], v[138:141], v216, v217 op_sel_hi:[0,0,0]
	s_setprio 0
	s_barrier
	s_mov_b32 m0, s55
	v_lshl_add_u64 v[214:215], s[30:31], 0, v[198:199]
	s_add_u32 s6, s30, 0x20000
	ds_read_b128 v[58:61], v234 offset:16384
	ds_read_b128 v[62:65], v234 offset:17408
	ds_read_b128 v[50:53], v234 offset:18432
	ds_read_b128 v[54:57], v234 offset:19456
	ds_read_b128 v[42:45], v234 offset:20480
	ds_read_b128 v[46:49], v234 offset:21504
	ds_read_b128 v[34:37], v234 offset:22528
	ds_read_b128 v[38:41], v234 offset:23552
	global_load_lds_dwordx4 v[214:215], off
	v_lshl_add_u64 v[212:213], s[30:31], 0, v[200:201]
	s_mov_b32 m0, s56
	s_addc_u32 s7, s31, 0
	global_load_lds_dwordx4 v[212:213], off
	v_lshl_add_u64 v[242:243], s[6:7], 0, v[198:199]
	s_mov_b32 m0, s58
	s_andn2_b64 vcc, exec, s[26:27]
	global_load_lds_dwordx4 v[242:243], off
	v_lshl_add_u64 v[242:243], s[6:7], 0, v[200:201]
	s_add_i32 m0, s58, 0x2000
	v_cmp_ne_u32_e64 s[6:7], 1, v203
	global_load_lds_dwordx4 v[242:243], off
	s_mov_b32 m0, s44
	s_nop 0
	global_load_lds_dwordx4 v66, s[34:35]
	s_mov_b32 m0, s45
	s_nop 0
	global_load_lds_dwordx4 v68, s[34:35]
	s_waitcnt vmcnt(8)
	s_waitcnt lgkmcnt(0)
	s_barrier
	s_cbranch_vccnz .LBB0_737
	s_setprio 1
	s_waitcnt lgkmcnt(0)
	v_mfma_scale_f32_16x16x128_f8f6f4 v[122:125], v[26:33], v[58:65], v[122:125], v216, v217 op_sel_hi:[0,0,0]
	v_mfma_scale_f32_16x16x128_f8f6f4 v[130:133], v[18:25], v[58:65], v[130:133], v216, v217 op_sel_hi:[0,0,0]
	v_mfma_scale_f32_16x16x128_f8f6f4 v[106:109], v[26:33], v[50:57], v[106:109], v216, v217 op_sel_hi:[0,0,0]
	v_mfma_scale_f32_16x16x128_f8f6f4 v[114:117], v[18:25], v[50:57], v[114:117], v216, v217 op_sel_hi:[0,0,0]
	v_mfma_scale_f32_16x16x128_f8f6f4 v[86:89], v[26:33], v[42:49], v[86:89], v216, v217 op_sel_hi:[0,0,0]
	v_mfma_scale_f32_16x16x128_f8f6f4 v[94:97], v[18:25], v[42:49], v[94:97], v216, v217 op_sel_hi:[0,0,0]
	v_mfma_scale_f32_16x16x128_f8f6f4 v[70:73], v[26:33], v[34:41], v[70:73], v216, v217 op_sel_hi:[0,0,0]
	v_mfma_scale_f32_16x16x128_f8f6f4 v[78:81], v[18:25], v[34:41], v[78:81], v216, v217 op_sel_hi:[0,0,0]
	s_setprio 0
	s_setprio 1
	v_mfma_scale_f32_16x16x128_f8f6f4 v[118:121], v[10:17], v[58:65], v[118:121], v216, v217 op_sel_hi:[0,0,0]
	v_mfma_scale_f32_16x16x128_f8f6f4 v[126:129], v[2:9], v[58:65], v[126:129], v216, v217 op_sel_hi:[0,0,0]
	v_mfma_scale_f32_16x16x128_f8f6f4 v[102:105], v[10:17], v[50:57], v[102:105], v216, v217 op_sel_hi:[0,0,0]
	v_mfma_scale_f32_16x16x128_f8f6f4 v[110:113], v[2:9], v[50:57], v[110:113], v216, v217 op_sel_hi:[0,0,0]
	v_mfma_scale_f32_16x16x128_f8f6f4 v[90:93], v[10:17], v[42:49], v[90:93], v216, v217 op_sel_hi:[0,0,0]
	v_mfma_scale_f32_16x16x128_f8f6f4 v[98:101], v[2:9], v[42:49], v[98:101], v216, v217 op_sel_hi:[0,0,0]
	v_mfma_scale_f32_16x16x128_f8f6f4 v[74:77], v[10:17], v[34:41], v[74:77], v216, v217 op_sel_hi:[0,0,0]
	v_mfma_scale_f32_16x16x128_f8f6f4 v[82:85], v[2:9], v[34:41], v[82:85], v216, v217 op_sel_hi:[0,0,0]
	s_setprio 0
; #define PG8_STAGE(bufoff, gbase, voff) do { _Pragma("unroll") for (int _i = 0; _i < 2; ++_i) \
;         __builtin_amdgcn_global_load_lds((const unsigned*)((const char*)(gbase) + (voff)[_i]), (LAS unsigned*)(lds + (bufoff) + ldsw + _i * 8192), 16, 0, 0); } while (0)
; #define PG8_LDA(dst, b, h) do { _Pragma("unroll") for (int m = 0; m < 4; ++m) _Pragma("unroll") for (int k = 0; k < 2; ++k) dst[m][k] = *(const LAS bf16x8*)(lds + PG8_SA(b, h) + aoff + m * 2048 + k * 1024); } while (0)
; #define PG8_LDB(dst, b, h) do { _Pragma("unroll") for (int n = 0; n < 2; ++n) _Pragma("unroll") for (int k = 0; k < 2; ++k) dst[n][k] = *(const LAS bf16x8*)(lds + PG8_SB(b, h) + boff + n * 2048 + k * 1024); } while (0)
; #define PG8_WAIT_V(n) asm volatile("s_waitcnt vmcnt(" #n ")" ::: "memory")
; #define PG8_WAIT_L(n) asm volatile("s_waitcnt lgkmcnt(" #n ")" ::: "memory")
; #define PG8_BAR __builtin_amdgcn_s_barrier()
; #define PG8_SCHED __builtin_amdgcn_sched_barrier(0)
;     ...
;             if constexpr (SP2) {
;             PG8_LDB(B0, 0, 0); PG8_LDB(B1, 0, 1); PG8_SCHED; PG8_LDA(At, 0, 0); PG8_STAGE(PG8_SA(1, 1), a1 + ah, VA1);
;             PG8_WAIT_V(8); PG8_WAIT_L(0); PG8_BAR; PG8_MMA(0, 0, At, B0); PG8_MMA(0, 1, At, B1); PG8_BAR; PG8_SCHED;
;             PG8_LDA(At, 0, 1); PG8_STAGE(PG8_SB(0, 0), b2, voffB); PG8_STAGE(PG8_SB(0, 1), b2 + bstep, voffB); PG8_STAGE(PG8_SA(0, 0), a2, v2[0]);
;             PG8_WAIT_V(8); PG8_WAIT_L(0); PG8_BAR; if (full) { PG8_MMA(1, 0, At, B0); PG8_MMA(1, 1, At, B1); } PG8_BAR; PG8_SCHED;
;             PG8_LDB(B0, 1, 0); PG8_LDB(B1, 1, 1); PG8_SCHED; PG8_LDA(At, 1, 0); PG8_STAGE(PG8_SA(0, 1), a2 + ah, v2[1]);
;             PG8_WAIT_V(8); PG8_WAIT_L(0); PG8_BAR; PG8_MMA(0, 0, At, B0); PG8_MMA(0, 1, At, B1); PG8_BAR; PG8_SCHED;
;             PG8_LDA(At, 1, 1); PG8_STAGE(PG8_SB(1, 0), b3, voffB); PG8_STAGE(PG8_SB(1, 1), b3 + bstep, voffB); PG8_STAGE(PG8_SA(1, 0), a3, v2[0]);
;             PG8_WAIT_V(8); PG8_WAIT_L(0); PG8_BAR; if (full) { PG8_MMA(1, 0, At, B0); PG8_MMA(1, 1, At, B1); } PG8_BAR; PG8_SCHED;
.LBB0_737:
	v_mov_b32_e32 v69, v67
	v_lshl_add_u64 v[242:243], s[34:35], 0, v[66:67]
	v_lshl_add_u64 v[68:69], s[34:35], 0, v[68:69]
	v_cndmask_b32_e64 v66, v202, v238, s[4:5]
	v_cndmask_b32_e64 v205, v204, v239, s[4:5]
	s_barrier
	s_add_i32 s4, 0, 0x18000
	s_add_i32 s75, 0, 0x1c000
	v_add_u32_e32 v2, s4, v223
	v_add_u32_e32 v6, s75, v223
	ds_read_b128 v[26:29], v2
	ds_read_b128 v[30:33], v2 offset:1024
	ds_read_b128 v[18:21], v2 offset:2048
	ds_read_b128 v[22:25], v2 offset:3072
	ds_read_b128 v[10:13], v6
	ds_read_b128 v[14:17], v6 offset:1024
	ds_read_b128 v[2:5], v6 offset:2048
	ds_read_b128 v[6:9], v6 offset:3072
	s_mov_b32 m0, s46
	ds_read_b128 v[34:37], v234 offset:32768
	ds_read_b128 v[38:41], v234 offset:33792
	ds_read_b128 v[42:45], v234 offset:34816
	ds_read_b128 v[46:49], v234 offset:35840
	ds_read_b128 v[50:53], v234 offset:36864
	ds_read_b128 v[54:57], v234 offset:37888
	ds_read_b128 v[58:61], v234 offset:38912
	ds_read_b128 v[62:65], v234 offset:39936
	global_load_lds_dwordx4 v66, s[34:35]
	s_mov_b32 m0, s47
	s_nop 0
	global_load_lds_dwordx4 v205, s[34:35]
	s_waitcnt vmcnt(8)
	s_waitcnt lgkmcnt(0)
	s_barrier
	s_setprio 1
	s_waitcnt lgkmcnt(0)
	v_mfma_scale_f32_16x16x128_f8f6f4 v[186:189], v[26:33], v[34:41], v[186:189], v216, v217 op_sel_hi:[0,0,0]
	v_mfma_scale_f32_16x16x128_f8f6f4 v[194:197], v[18:25], v[34:41], v[194:197], v216, v217 op_sel_hi:[0,0,0]
	v_mfma_scale_f32_16x16x128_f8f6f4 v[170:173], v[26:33], v[42:49], v[170:173], v216, v217 op_sel_hi:[0,0,0]
	v_mfma_scale_f32_16x16x128_f8f6f4 v[178:181], v[18:25], v[42:49], v[178:181], v216, v217 op_sel_hi:[0,0,0]
	v_mfma_scale_f32_16x16x128_f8f6f4 v[154:157], v[26:33], v[50:57], v[154:157], v216, v217 op_sel_hi:[0,0,0]
	v_mfma_scale_f32_16x16x128_f8f6f4 v[162:165], v[18:25], v[50:57], v[162:165], v216, v217 op_sel_hi:[0,0,0]
	v_mfma_scale_f32_16x16x128_f8f6f4 v[142:145], v[26:33], v[58:65], v[142:145], v216, v217 op_sel_hi:[0,0,0]
	v_mfma_scale_f32_16x16x128_f8f6f4 v[146:149], v[18:25], v[58:65], v[146:149], v216, v217 op_sel_hi:[0,0,0]
	s_setprio 0
	s_setprio 1
	v_mfma_scale_f32_16x16x128_f8f6f4 v[182:185], v[10:17], v[34:41], v[182:185], v216, v217 op_sel_hi:[0,0,0]
	v_mfma_scale_f32_16x16x128_f8f6f4 v[190:193], v[2:9], v[34:41], v[190:193], v216, v217 op_sel_hi:[0,0,0]
	v_mfma_scale_f32_16x16x128_f8f6f4 v[166:169], v[10:17], v[42:49], v[166:169], v216, v217 op_sel_hi:[0,0,0]
	v_mfma_scale_f32_16x16x128_f8f6f4 v[174:177], v[2:9], v[42:49], v[174:177], v216, v217 op_sel_hi:[0,0,0]
	v_mfma_scale_f32_16x16x128_f8f6f4 v[150:153], v[10:17], v[50:57], v[150:153], v216, v217 op_sel_hi:[0,0,0]
	v_mfma_scale_f32_16x16x128_f8f6f4 v[158:161], v[2:9], v[50:57], v[158:161], v216, v217 op_sel_hi:[0,0,0]
	v_mfma_scale_f32_16x16x128_f8f6f4 v[134:137], v[10:17], v[58:65], v[134:137], v216, v217 op_sel_hi:[0,0,0]
	v_mfma_scale_f32_16x16x128_f8f6f4 v[138:141], v[2:9], v[58:65], v[138:141], v216, v217 op_sel_hi:[0,0,0]
	s_setprio 0
	s_barrier
	s_add_i32 s4, s4, s40
	v_lshl_add_u64 v[214:215], v[214:215], 0, s[14:15]
	s_mov_b32 m0, s4
	ds_read_b128 v[58:61], v234 offset:49152
	ds_read_b128 v[62:65], v234 offset:50176
	ds_read_b128 v[50:53], v234 offset:51200
	ds_read_b128 v[54:57], v234 offset:52224
	ds_read_b128 v[42:45], v234 offset:53248
	ds_read_b128 v[46:49], v234 offset:54272
	ds_read_b128 v[34:37], v234 offset:55296
	ds_read_b128 v[38:41], v234 offset:56320
	global_load_lds_dwordx4 v[214:215], off
	s_add_i32 m0, s4, 0x2000
	s_add_u32 s4, s30, 0x20080
	v_lshl_add_u64 v[212:213], v[212:213], 0, s[14:15]
	s_addc_u32 s5, s31, 0
	s_add_i32 s30, s75, s40
	global_load_lds_dwordx4 v[212:213], off
	v_lshl_add_u64 v[212:213], s[4:5], 0, v[198:199]
	s_mov_b32 m0, s30
	v_lshl_add_u64 v[68:69], v[68:69], 0, s[14:15]
	global_load_lds_dwordx4 v[212:213], off
	v_lshl_add_u64 v[212:213], s[4:5], 0, v[200:201]
	s_add_i32 m0, s30, 0x2000
	s_and_b64 vcc, exec, s[6:7]
	global_load_lds_dwordx4 v[212:213], off
	v_lshl_add_u64 v[212:213], v[242:243], 0, s[14:15]
	s_mov_b32 m0, s49
	s_nop 0
	global_load_lds_dwordx4 v[212:213], off
	s_mov_b32 m0, s50
	s_nop 0
	global_load_lds_dwordx4 v[68:69], off
	s_waitcnt vmcnt(8)
	s_waitcnt lgkmcnt(0)
	s_barrier
	s_cbranch_vccnz .LBB0_734
	s_setprio 1
	s_waitcnt lgkmcnt(0)
	v_mfma_scale_f32_16x16x128_f8f6f4 v[122:125], v[26:33], v[58:65], v[122:125], v216, v217 op_sel_hi:[0,0,0]
	v_mfma_scale_f32_16x16x128_f8f6f4 v[130:133], v[18:25], v[58:65], v[130:133], v216, v217 op_sel_hi:[0,0,0]
	v_mfma_scale_f32_16x16x128_f8f6f4 v[106:109], v[26:33], v[50:57], v[106:109], v216, v217 op_sel_hi:[0,0,0]
	v_mfma_scale_f32_16x16x128_f8f6f4 v[114:117], v[18:25], v[50:57], v[114:117], v216, v217 op_sel_hi:[0,0,0]
	v_mfma_scale_f32_16x16x128_f8f6f4 v[86:89], v[26:33], v[42:49], v[86:89], v216, v217 op_sel_hi:[0,0,0]
	v_mfma_scale_f32_16x16x128_f8f6f4 v[94:97], v[18:25], v[42:49], v[94:97], v216, v217 op_sel_hi:[0,0,0]
	v_mfma_scale_f32_16x16x128_f8f6f4 v[70:73], v[26:33], v[34:41], v[70:73], v216, v217 op_sel_hi:[0,0,0]
	v_mfma_scale_f32_16x16x128_f8f6f4 v[78:81], v[18:25], v[34:41], v[78:81], v216, v217 op_sel_hi:[0,0,0]
	s_setprio 0
	s_setprio 1
	v_mfma_scale_f32_16x16x128_f8f6f4 v[118:121], v[10:17], v[58:65], v[118:121], v216, v217 op_sel_hi:[0,0,0]
	v_mfma_scale_f32_16x16x128_f8f6f4 v[126:129], v[2:9], v[58:65], v[126:129], v216, v217 op_sel_hi:[0,0,0]
	v_mfma_scale_f32_16x16x128_f8f6f4 v[102:105], v[10:17], v[50:57], v[102:105], v216, v217 op_sel_hi:[0,0,0]
	v_mfma_scale_f32_16x16x128_f8f6f4 v[110:113], v[2:9], v[50:57], v[110:113], v216, v217 op_sel_hi:[0,0,0]
	v_mfma_scale_f32_16x16x128_f8f6f4 v[90:93], v[10:17], v[42:49], v[90:93], v216, v217 op_sel_hi:[0,0,0]
	v_mfma_scale_f32_16x16x128_f8f6f4 v[98:101], v[2:9], v[42:49], v[98:101], v216, v217 op_sel_hi:[0,0,0]
	v_mfma_scale_f32_16x16x128_f8f6f4 v[74:77], v[10:17], v[34:41], v[74:77], v216, v217 op_sel_hi:[0,0,0]
	v_mfma_scale_f32_16x16x128_f8f6f4 v[82:85], v[2:9], v[34:41], v[82:85], v216, v217 op_sel_hi:[0,0,0]
	s_setprio 0
	s_branch .LBB0_734

; #define PG8_STAGE(bufoff, gbase, voff) do { _Pragma("unroll") for (int _i = 0; _i < 2; ++_i) \
;         __builtin_amdgcn_global_load_lds((const unsigned*)((const char*)(gbase) + (voff)[_i]), (LAS unsigned*)(lds + (bufoff) + ldsw + _i * 8192), 16, 0, 0); } while (0)
; #define PG8_LDA(dst, b, h) do { _Pragma("unroll") for (int m = 0; m < 4; ++m) _Pragma("unroll") for (int k = 0; k < 2; ++k) dst[m][k] = *(const LAS bf16x8*)(lds + PG8_SA(b, h) + aoff + m * 2048 + k * 1024); } while (0)
; #define PG8_LDB(dst, b, h) do { _Pragma("unroll") for (int n = 0; n < 2; ++n) _Pragma("unroll") for (int k = 0; k < 2; ++k) dst[n][k] = *(const LAS bf16x8*)(lds + PG8_SB(b, h) + boff + n * 2048 + k * 1024); } while (0)
; #define PG8_WAIT_V(n) asm volatile("s_waitcnt vmcnt(" #n ")" ::: "memory")
; #define PG8_WAIT_L(n) asm volatile("s_waitcnt lgkmcnt(" #n ")" ::: "memory")
; #define PG8_BAR __builtin_amdgcn_s_barrier()
; #define PG8_SCHED __builtin_amdgcn_sched_barrier(0)
;     ...
;             if constexpr (SP2) {
;             PG8_LDB(B0, 0, 0); PG8_LDB(B1, 0, 1); PG8_SCHED; PG8_LDA(At, 0, 0); PG8_STAGE(PG8_SA(1, 1), a1 + ah, VA1);
;             PG8_WAIT_V(8); PG8_WAIT_L(0); PG8_BAR; PG8_MMA(0, 0, At, B0); PG8_MMA(0, 1, At, B1); PG8_BAR; PG8_SCHED;
;             PG8_LDA(At, 0, 1); PG8_STAGE(PG8_SB(0, 0), b2, voffB); PG8_STAGE(PG8_SB(0, 1), b2 + bstep, voffB); PG8_STAGE(PG8_SA(0, 0), a2, v2[0]);
;             PG8_WAIT_V(8); PG8_WAIT_L(0); PG8_BAR; if (full) { PG8_MMA(1, 0, At, B0); PG8_MMA(1, 1, At, B1); } PG8_BAR; PG8_SCHED;
;             PG8_LDB(B0, 1, 0); PG8_LDB(B1, 1, 1); PG8_SCHED; PG8_LDA(At, 1, 0); PG8_STAGE(PG8_SA(0, 1), a2 + ah, v2[1]);
;             PG8_WAIT_V(8); PG8_WAIT_L(0); PG8_BAR; PG8_MMA(0, 0, At, B0); PG8_MMA(0, 1, At, B1); PG8_BAR; PG8_SCHED;
;             PG8_LDA(At, 1, 1); PG8_STAGE(PG8_SB(1, 0), b3, voffB); PG8_STAGE(PG8_SB(1, 1), b3 + bstep, voffB); PG8_STAGE(PG8_SA(1, 0), a3, v2[0]);
;             PG8_WAIT_V(8); PG8_WAIT_L(0); PG8_BAR; if (full) { PG8_MMA(1, 0, At, B0); PG8_MMA(1, 1, At, B1); } PG8_BAR; PG8_SCHED;
.LBB0_841:
	s_add_u32 s4, s4, 0x8000
	s_addc_u32 s5, s5, 0
	s_barrier
	s_add_i32 s35, 0, 0x18000
	s_add_i32 s36, 0, 0x1c000
	v_add_u32_e32 v2, s35, v247
	v_add_u32_e32 v6, s36, v247
	ds_read_b128 v[26:29], v2
	ds_read_b128 v[30:33], v2 offset:1024
	ds_read_b128 v[18:21], v2 offset:2048
	ds_read_b128 v[22:25], v2 offset:3072
	ds_read_b128 v[10:13], v6
	ds_read_b128 v[14:17], v6 offset:1024
	ds_read_b128 v[2:5], v6 offset:2048
	ds_read_b128 v[6:9], v6 offset:3072
	s_mov_b32 m0, s15
	v_lshl_add_u64 v[250:251], s[4:5], 0, v[200:201]
	ds_read_b128 v[34:37], v223 offset:32768
	ds_read_b128 v[38:41], v223 offset:33792
	ds_read_b128 v[42:45], v223 offset:34816
	ds_read_b128 v[46:49], v223 offset:35840
	ds_read_b128 v[50:53], v223 offset:36864
	ds_read_b128 v[54:57], v223 offset:37888
	ds_read_b128 v[58:61], v223 offset:38912
	ds_read_b128 v[62:65], v223 offset:39936
	global_load_lds_dwordx4 v[250:251], off
	v_lshl_add_u64 v[250:251], s[4:5], 0, v[202:203]
	s_mov_b32 m0, s16
	s_nop 0
	global_load_lds_dwordx4 v[250:251], off
	s_waitcnt vmcnt(8)
	s_waitcnt lgkmcnt(0)
	s_barrier
	s_setprio 1
	s_waitcnt lgkmcnt(0)
	v_mfma_scale_f32_16x16x128_f8f6f4 v[172:175], v[26:33], v[34:41], v[172:175], v1, v246 op_sel_hi:[0,0,0]
	v_mfma_scale_f32_16x16x128_f8f6f4 v[176:179], v[18:25], v[34:41], v[176:179], v1, v246 op_sel_hi:[0,0,0]
	v_mfma_scale_f32_16x16x128_f8f6f4 v[168:171], v[26:33], v[42:49], v[168:171], v1, v246 op_sel_hi:[0,0,0]
	v_mfma_scale_f32_16x16x128_f8f6f4 v[164:167], v[18:25], v[42:49], v[164:167], v1, v246 op_sel_hi:[0,0,0]
	v_mfma_scale_f32_16x16x128_f8f6f4 v[144:147], v[26:33], v[50:57], v[144:147], v1, v246 op_sel_hi:[0,0,0]
	v_mfma_scale_f32_16x16x128_f8f6f4 v[136:139], v[18:25], v[50:57], v[136:139], v1, v246 op_sel_hi:[0,0,0]
	v_mfma_scale_f32_16x16x128_f8f6f4 v[116:119], v[26:33], v[58:65], v[116:119], v1, v246 op_sel_hi:[0,0,0]
	v_mfma_scale_f32_16x16x128_f8f6f4 v[112:115], v[18:25], v[58:65], v[112:115], v1, v246 op_sel_hi:[0,0,0]
	s_setprio 0
	s_setprio 1
	v_mfma_scale_f32_16x16x128_f8f6f4 v[188:191], v[10:17], v[34:41], v[188:191], v1, v246 op_sel_hi:[0,0,0]
	v_mfma_scale_f32_16x16x128_f8f6f4 v[192:195], v[2:9], v[34:41], v[192:195], v1, v246 op_sel_hi:[0,0,0]
	v_mfma_scale_f32_16x16x128_f8f6f4 v[184:187], v[10:17], v[42:49], v[184:187], v1, v246 op_sel_hi:[0,0,0]
	v_mfma_scale_f32_16x16x128_f8f6f4 v[180:183], v[2:9], v[42:49], v[180:183], v1, v246 op_sel_hi:[0,0,0]
	v_mfma_scale_f32_16x16x128_f8f6f4 v[152:155], v[10:17], v[50:57], v[152:155], v1, v246 op_sel_hi:[0,0,0]
	v_mfma_scale_f32_16x16x128_f8f6f4 v[148:151], v[2:9], v[50:57], v[148:151], v1, v246 op_sel_hi:[0,0,0]
	v_mfma_scale_f32_16x16x128_f8f6f4 v[120:123], v[10:17], v[58:65], v[120:123], v1, v246 op_sel_hi:[0,0,0]
	v_mfma_scale_f32_16x16x128_f8f6f4 v[80:83], v[2:9], v[58:65], v[80:83], v1, v246 op_sel_hi:[0,0,0]
	s_setprio 0
	s_barrier
	s_add_i32 s4, s35, s8
	v_lshl_add_u64 v[250:251], v[240:241], 0, s[48:49]
	s_mov_b32 m0, s4
	ds_read_b128 v[58:61], v223 offset:49152
	ds_read_b128 v[62:65], v223 offset:50176
	ds_read_b128 v[50:53], v223 offset:51200
	ds_read_b128 v[54:57], v223 offset:52224
	ds_read_b128 v[42:45], v223 offset:53248
	ds_read_b128 v[46:49], v223 offset:54272
	ds_read_b128 v[34:37], v223 offset:55296
	ds_read_b128 v[38:41], v223 offset:56320
	global_load_lds_dwordx4 v[250:251], off
	v_lshl_add_u64 v[250:251], v[238:239], 0, s[48:49]
	s_add_i32 m0, s4, 0x2000
	s_add_i32 s4, s36, s8
	global_load_lds_dwordx4 v[250:251], off
	v_lshl_add_u64 v[240:241], v[240:241], 0, s[50:51]
	s_mov_b32 m0, s4
	v_lshl_add_u64 v[238:239], v[238:239], 0, s[50:51]
	global_load_lds_dwordx4 v[240:241], off
	s_add_i32 m0, s4, 0x2000
	s_andn2_b64 vcc, exec, s[90:91]
	global_load_lds_dwordx4 v[238:239], off
	v_lshl_add_u64 v[238:239], v[242:243], 0, s[48:49]
	s_mov_b32 m0, s20
	s_nop 0
	global_load_lds_dwordx4 v[238:239], off
	v_lshl_add_u64 v[238:239], v[244:245], 0, s[48:49]
	s_mov_b32 m0, s21
	s_nop 0
	global_load_lds_dwordx4 v[238:239], off
	s_waitcnt vmcnt(8)
	s_waitcnt lgkmcnt(0)
	s_barrier
	s_cbranch_vccnz .LBB0_843
	s_setprio 1
	s_waitcnt lgkmcnt(0)
	v_mfma_scale_f32_16x16x128_f8f6f4 v[128:131], v[26:33], v[58:65], v[128:131], v1, v246 op_sel_hi:[0,0,0]
	v_mfma_scale_f32_16x16x128_f8f6f4 v[124:127], v[18:25], v[58:65], v[124:127], v1, v246 op_sel_hi:[0,0,0]
	v_mfma_scale_f32_16x16x128_f8f6f4 v[108:111], v[26:33], v[50:57], v[108:111], v1, v246 op_sel_hi:[0,0,0]
	v_mfma_scale_f32_16x16x128_f8f6f4 v[104:107], v[18:25], v[50:57], v[104:107], v1, v246 op_sel_hi:[0,0,0]
	v_mfma_scale_f32_16x16x128_f8f6f4 v[92:95], v[26:33], v[42:49], v[92:95], v1, v246 op_sel_hi:[0,0,0]
	v_mfma_scale_f32_16x16x128_f8f6f4 v[84:87], v[18:25], v[42:49], v[84:87], v1, v246 op_sel_hi:[0,0,0]
	v_mfma_scale_f32_16x16x128_f8f6f4 v[76:79], v[26:33], v[34:41], v[76:79], v1, v246 op_sel_hi:[0,0,0]
	v_mfma_scale_f32_16x16x128_f8f6f4 v[72:75], v[18:25], v[34:41], v[72:75], v1, v246 op_sel_hi:[0,0,0]
	s_setprio 0
	s_setprio 1
	v_mfma_scale_f32_16x16x128_f8f6f4 v[160:163], v[10:17], v[58:65], v[160:163], v1, v246 op_sel_hi:[0,0,0]
	v_mfma_scale_f32_16x16x128_f8f6f4 v[156:159], v[2:9], v[58:65], v[156:159], v1, v246 op_sel_hi:[0,0,0]
	v_mfma_scale_f32_16x16x128_f8f6f4 v[140:143], v[10:17], v[50:57], v[140:143], v1, v246 op_sel_hi:[0,0,0]
	v_mfma_scale_f32_16x16x128_f8f6f4 v[132:135], v[2:9], v[50:57], v[132:135], v1, v246 op_sel_hi:[0,0,0]
	v_mfma_scale_f32_16x16x128_f8f6f4 v[100:103], v[10:17], v[42:49], v[100:103], v1, v246 op_sel_hi:[0,0,0]
	v_mfma_scale_f32_16x16x128_f8f6f4 v[96:99], v[2:9], v[42:49], v[96:99], v1, v246 op_sel_hi:[0,0,0]
	v_mfma_scale_f32_16x16x128_f8f6f4 v[88:91], v[10:17], v[34:41], v[88:91], v1, v246 op_sel_hi:[0,0,0]
	v_mfma_scale_f32_16x16x128_f8f6f4 v[68:71], v[2:9], v[34:41], v[68:71], v1, v246 op_sel_hi:[0,0,0]
	s_setprio 0

; #define PG8_STAGE(bufoff, gbase, voff) do { _Pragma("unroll") for (int _i = 0; _i < 2; ++_i) \
;         __builtin_amdgcn_global_load_lds((const unsigned*)((const char*)(gbase) + (voff)[_i]), (LAS unsigned*)(lds + (bufoff) + ldsw + _i * 8192), 16, 0, 0); } while (0)
; #define PG8_LDA(dst, b, h) do { _Pragma("unroll") for (int m = 0; m < 4; ++m) _Pragma("unroll") for (int k = 0; k < 2; ++k) dst[m][k] = *(const LAS bf16x8*)(lds + PG8_SA(b, h) + aoff + m * 2048 + k * 1024); } while (0)
; #define PG8_LDB(dst, b, h) do { _Pragma("unroll") for (int n = 0; n < 2; ++n) _Pragma("unroll") for (int k = 0; k < 2; ++k) dst[n][k] = *(const LAS bf16x8*)(lds + PG8_SB(b, h) + boff + n * 2048 + k * 1024); } while (0)
; #define PG8_WAIT_V(n) asm volatile("s_waitcnt vmcnt(" #n ")" ::: "memory")
; #define PG8_WAIT_L(n) asm volatile("s_waitcnt lgkmcnt(" #n ")" ::: "memory")
; #define PG8_BAR __builtin_amdgcn_s_barrier()
; #define PG8_SCHED __builtin_amdgcn_sched_barrier(0)
;     ...
;             const bool last = (t == nt - 2);
;             const char* a1 = cA + (size_t)(t + 1) * kstep;
;             const char* a2 = last ? nA : cA + (size_t)(t + 2) * kstep; const char* b2 = last ? nB : cB + (size_t)(t + 2) * kstep;
;             const char* a3 = a2 + kstep; const char* b3 = b2 + kstep;
;             unsigned v2[2][2];
;             if constexpr (GATHER) { v2[0][0] = last ? vn[0][0] : va[0][0]; v2[0][1] = last ? vn[0][1] : va[0][1]; v2[1][0] = last ? vn[1][0] : va[1][0]; v2[1][1] = last ? vn[1][1] : va[1][1]; }
;             else { v2[0][0] = va[0][0]; v2[0][1] = va[0][1]; v2[1][0] = va[0][0]; v2[1][1] = va[0][1]; }
;             if constexpr (SP2) {
;             PG8_LDB(B0, 0, 0); PG8_LDB(B1, 0, 1); PG8_SCHED; PG8_LDA(At, 0, 0); PG8_STAGE(PG8_SA(1, 1), a1 + ah, VA1);
;             PG8_WAIT_V(8); PG8_WAIT_L(0); PG8_BAR; PG8_MMA(0, 0, At, B0); PG8_MMA(0, 1, At, B1); PG8_BAR; PG8_SCHED;
;             PG8_LDA(At, 0, 1); PG8_STAGE(PG8_SB(0, 0), b2, voffB); PG8_STAGE(PG8_SB(0, 1), b2 + bstep, voffB); PG8_STAGE(PG8_SA(0, 0), a2, v2[0]);
;             PG8_WAIT_V(8); PG8_WAIT_L(0); PG8_BAR; if (full) { PG8_MMA(1, 0, At, B0); PG8_MMA(1, 1, At, B1); } PG8_BAR; PG8_SCHED;
.LBB0_954:
	ds_read_b128 v[26:29], v232
	ds_read_b128 v[30:33], v232 offset:1024
	ds_read_b128 v[18:21], v232 offset:2048
	ds_read_b128 v[22:25], v232 offset:3072
	ds_read_b128 v[10:13], v233
	ds_read_b128 v[14:17], v233 offset:1024
	ds_read_b128 v[2:5], v233 offset:2048
	ds_read_b128 v[6:9], v233 offset:3072
	s_add_u32 s4, s90, s94
	s_addc_u32 s5, s91, s95
	s_add_u32 s42, s4, 0x319d0100
	s_addc_u32 s43, s5, 0
	s_add_u32 s96, s37, s94
	s_addc_u32 s97, s18, s95
	s_cmpk_eq_i32 s94, 0x300
	s_cselect_b64 s[40:41], -1, 0
	s_and_b64 s[4:5], s[40:41], exec
	v_cndmask_b32_e64 v66, v240, v236, s[40:41]
	s_cselect_b32 s5, s45, s43
	s_cselect_b32 s4, s44, s42
	v_cndmask_b32_e64 v68, v206, v238, s[40:41]
	s_cselect_b32 s97, s57, s97
	s_cselect_b32 s96, s36, s96
	s_mov_b32 m0, s23
	v_lshl_add_u64 v[212:213], v[210:211], 0, s[94:95]
	ds_read_b128 v[34:37], v234
	ds_read_b128 v[38:41], v234 offset:1024
	ds_read_b128 v[42:45], v234 offset:2048
	ds_read_b128 v[46:49], v234 offset:3072
	ds_read_b128 v[50:53], v234 offset:4096
	ds_read_b128 v[54:57], v234 offset:5120
	ds_read_b128 v[58:61], v234 offset:6144
	ds_read_b128 v[62:65], v234 offset:7168
	global_load_lds_dwordx4 v[212:213], off
	v_lshl_add_u64 v[212:213], v[208:209], 0, s[94:95]
	s_mov_b32 m0, s20
	s_nop 0
	global_load_lds_dwordx4 v[212:213], off
	s_waitcnt vmcnt(8)
	s_waitcnt lgkmcnt(0)
	s_barrier
	s_setprio 1
	s_waitcnt lgkmcnt(0)
	v_mfma_scale_f32_16x16x128_f8f6f4 v[186:189], v[26:33], v[34:41], v[186:189], v216, v217 op_sel_hi:[0,0,0]
	v_mfma_scale_f32_16x16x128_f8f6f4 v[194:197], v[18:25], v[34:41], v[194:197], v216, v217 op_sel_hi:[0,0,0]
	v_mfma_scale_f32_16x16x128_f8f6f4 v[170:173], v[26:33], v[42:49], v[170:173], v216, v217 op_sel_hi:[0,0,0]
	v_mfma_scale_f32_16x16x128_f8f6f4 v[178:181], v[18:25], v[42:49], v[178:181], v216, v217 op_sel_hi:[0,0,0]
	v_mfma_scale_f32_16x16x128_f8f6f4 v[154:157], v[26:33], v[50:57], v[154:157], v216, v217 op_sel_hi:[0,0,0]
	v_mfma_scale_f32_16x16x128_f8f6f4 v[162:165], v[18:25], v[50:57], v[162:165], v216, v217 op_sel_hi:[0,0,0]
	v_mfma_scale_f32_16x16x128_f8f6f4 v[138:141], v[26:33], v[58:65], v[138:141], v216, v217 op_sel_hi:[0,0,0]
	v_mfma_scale_f32_16x16x128_f8f6f4 v[146:149], v[18:25], v[58:65], v[146:149], v216, v217 op_sel_hi:[0,0,0]
	s_setprio 0
	s_setprio 1
	v_mfma_scale_f32_16x16x128_f8f6f4 v[182:185], v[10:17], v[34:41], v[182:185], v216, v217 op_sel_hi:[0,0,0]
	v_mfma_scale_f32_16x16x128_f8f6f4 v[190:193], v[2:9], v[34:41], v[190:193], v216, v217 op_sel_hi:[0,0,0]
	v_mfma_scale_f32_16x16x128_f8f6f4 v[166:169], v[10:17], v[42:49], v[166:169], v216, v217 op_sel_hi:[0,0,0]
	v_mfma_scale_f32_16x16x128_f8f6f4 v[174:177], v[2:9], v[42:49], v[174:177], v216, v217 op_sel_hi:[0,0,0]
	v_mfma_scale_f32_16x16x128_f8f6f4 v[150:153], v[10:17], v[50:57], v[150:153], v216, v217 op_sel_hi:[0,0,0]
	v_mfma_scale_f32_16x16x128_f8f6f4 v[158:161], v[2:9], v[50:57], v[158:161], v216, v217 op_sel_hi:[0,0,0]
	v_mfma_scale_f32_16x16x128_f8f6f4 v[134:137], v[10:17], v[58:65], v[134:137], v216, v217 op_sel_hi:[0,0,0]
	v_mfma_scale_f32_16x16x128_f8f6f4 v[142:145], v[2:9], v[58:65], v[142:145], v216, v217 op_sel_hi:[0,0,0]
	s_setprio 0
	s_barrier
	s_mov_b32 m0, s25
	v_lshl_add_u64 v[214:215], s[96:97], 0, v[198:199]
	s_add_u32 s42, s96, 0x20000
	ds_read_b128 v[58:61], v234 offset:16384
	ds_read_b128 v[62:65], v234 offset:17408
	ds_read_b128 v[50:53], v234 offset:18432
	ds_read_b128 v[54:57], v234 offset:19456
	ds_read_b128 v[42:45], v234 offset:20480
	ds_read_b128 v[46:49], v234 offset:21504
	ds_read_b128 v[34:37], v234 offset:22528
	ds_read_b128 v[38:41], v234 offset:23552
	global_load_lds_dwordx4 v[214:215], off
	v_lshl_add_u64 v[212:213], s[96:97], 0, v[200:201]
	s_mov_b32 m0, s26
	s_addc_u32 s43, s97, 0
	global_load_lds_dwordx4 v[212:213], off
	v_lshl_add_u64 v[242:243], s[42:43], 0, v[198:199]
	s_mov_b32 m0, s27
	s_andn2_b64 vcc, exec, s[92:93]
	global_load_lds_dwordx4 v[242:243], off
	v_lshl_add_u64 v[242:243], s[42:43], 0, v[200:201]
	s_add_i32 m0, s27, 0x2000
	v_cmp_ne_u32_e64 s[42:43], 1, v203
	global_load_lds_dwordx4 v[242:243], off
	s_mov_b32 m0, s24
	s_nop 0
	global_load_lds_dwordx4 v66, s[4:5]
	s_mov_b32 m0, s14
	s_nop 0
	global_load_lds_dwordx4 v68, s[4:5]
	s_waitcnt vmcnt(8)
	s_waitcnt lgkmcnt(0)
	s_barrier
	s_cbranch_vccnz .LBB0_956
	s_setprio 1
	s_waitcnt lgkmcnt(0)
	v_mfma_scale_f32_16x16x128_f8f6f4 v[118:121], v[26:33], v[58:65], v[118:121], v216, v217 op_sel_hi:[0,0,0]
	v_mfma_scale_f32_16x16x128_f8f6f4 v[126:129], v[18:25], v[58:65], v[126:129], v216, v217 op_sel_hi:[0,0,0]
	v_mfma_scale_f32_16x16x128_f8f6f4 v[102:105], v[26:33], v[50:57], v[102:105], v216, v217 op_sel_hi:[0,0,0]
	v_mfma_scale_f32_16x16x128_f8f6f4 v[110:113], v[18:25], v[50:57], v[110:113], v216, v217 op_sel_hi:[0,0,0]
	v_mfma_scale_f32_16x16x128_f8f6f4 v[86:89], v[26:33], v[42:49], v[86:89], v216, v217 op_sel_hi:[0,0,0]
	v_mfma_scale_f32_16x16x128_f8f6f4 v[94:97], v[18:25], v[42:49], v[94:97], v216, v217 op_sel_hi:[0,0,0]
	v_mfma_scale_f32_16x16x128_f8f6f4 v[70:73], v[26:33], v[34:41], v[70:73], v216, v217 op_sel_hi:[0,0,0]
	v_mfma_scale_f32_16x16x128_f8f6f4 v[78:81], v[18:25], v[34:41], v[78:81], v216, v217 op_sel_hi:[0,0,0]
	s_setprio 0
	s_setprio 1
	v_mfma_scale_f32_16x16x128_f8f6f4 v[122:125], v[10:17], v[58:65], v[122:125], v216, v217 op_sel_hi:[0,0,0]
	v_mfma_scale_f32_16x16x128_f8f6f4 v[130:133], v[2:9], v[58:65], v[130:133], v216, v217 op_sel_hi:[0,0,0]
	v_mfma_scale_f32_16x16x128_f8f6f4 v[106:109], v[10:17], v[50:57], v[106:109], v216, v217 op_sel_hi:[0,0,0]
	v_mfma_scale_f32_16x16x128_f8f6f4 v[114:117], v[2:9], v[50:57], v[114:117], v216, v217 op_sel_hi:[0,0,0]
	v_mfma_scale_f32_16x16x128_f8f6f4 v[90:93], v[10:17], v[42:49], v[90:93], v216, v217 op_sel_hi:[0,0,0]
	v_mfma_scale_f32_16x16x128_f8f6f4 v[98:101], v[2:9], v[42:49], v[98:101], v216, v217 op_sel_hi:[0,0,0]
	v_mfma_scale_f32_16x16x128_f8f6f4 v[74:77], v[10:17], v[34:41], v[74:77], v216, v217 op_sel_hi:[0,0,0]
	v_mfma_scale_f32_16x16x128_f8f6f4 v[82:85], v[2:9], v[34:41], v[82:85], v216, v217 op_sel_hi:[0,0,0]
	s_setprio 0
; #define PG8_STAGE(bufoff, gbase, voff) do { _Pragma("unroll") for (int _i = 0; _i < 2; ++_i) \
;         __builtin_amdgcn_global_load_lds((const unsigned*)((const char*)(gbase) + (voff)[_i]), (LAS unsigned*)(lds + (bufoff) + ldsw + _i * 8192), 16, 0, 0); } while (0)
; #define PG8_LDA(dst, b, h) do { _Pragma("unroll") for (int m = 0; m < 4; ++m) _Pragma("unroll") for (int k = 0; k < 2; ++k) dst[m][k] = *(const LAS bf16x8*)(lds + PG8_SA(b, h) + aoff + m * 2048 + k * 1024); } while (0)
; #define PG8_LDB(dst, b, h) do { _Pragma("unroll") for (int n = 0; n < 2; ++n) _Pragma("unroll") for (int k = 0; k < 2; ++k) dst[n][k] = *(const LAS bf16x8*)(lds + PG8_SB(b, h) + boff + n * 2048 + k * 1024); } while (0)
; #define PG8_WAIT_V(n) asm volatile("s_waitcnt vmcnt(" #n ")" ::: "memory")
; #define PG8_WAIT_L(n) asm volatile("s_waitcnt lgkmcnt(" #n ")" ::: "memory")
; #define PG8_BAR __builtin_amdgcn_s_barrier()
; #define PG8_SCHED __builtin_amdgcn_sched_barrier(0)
;     ...
;             if constexpr (SP2) {
;             PG8_LDB(B0, 0, 0); PG8_LDB(B1, 0, 1); PG8_SCHED; PG8_LDA(At, 0, 0); PG8_STAGE(PG8_SA(1, 1), a1 + ah, VA1);
;             PG8_WAIT_V(8); PG8_WAIT_L(0); PG8_BAR; PG8_MMA(0, 0, At, B0); PG8_MMA(0, 1, At, B1); PG8_BAR; PG8_SCHED;
;             PG8_LDA(At, 0, 1); PG8_STAGE(PG8_SB(0, 0), b2, voffB); PG8_STAGE(PG8_SB(0, 1), b2 + bstep, voffB); PG8_STAGE(PG8_SA(0, 0), a2, v2[0]);
;             PG8_WAIT_V(8); PG8_WAIT_L(0); PG8_BAR; if (full) { PG8_MMA(1, 0, At, B0); PG8_MMA(1, 1, At, B1); } PG8_BAR; PG8_SCHED;
;             PG8_LDB(B0, 1, 0); PG8_LDB(B1, 1, 1); PG8_SCHED; PG8_LDA(At, 1, 0); PG8_STAGE(PG8_SA(0, 1), a2 + ah, v2[1]);
;             PG8_WAIT_V(8); PG8_WAIT_L(0); PG8_BAR; PG8_MMA(0, 0, At, B0); PG8_MMA(0, 1, At, B1); PG8_BAR; PG8_SCHED;
;             PG8_LDA(At, 1, 1); PG8_STAGE(PG8_SB(1, 0), b3, voffB); PG8_STAGE(PG8_SB(1, 1), b3 + bstep, voffB); PG8_STAGE(PG8_SA(1, 0), a3, v2[0]);
;             PG8_WAIT_V(8); PG8_WAIT_L(0); PG8_BAR; if (full) { PG8_MMA(1, 0, At, B0); PG8_MMA(1, 1, At, B1); } PG8_BAR; PG8_SCHED;
.LBB0_956:
	v_mov_b32_e32 v69, v67
	v_lshl_add_u64 v[242:243], s[4:5], 0, v[66:67]
	v_lshl_add_u64 v[68:69], s[4:5], 0, v[68:69]
	v_cndmask_b32_e64 v66, v202, v237, s[40:41]
	v_cndmask_b32_e64 v205, v204, v239, s[40:41]
	s_barrier
	s_add_i32 s40, 0, 0x18000
	s_add_i32 s41, 0, 0x1c000
	v_add_u32_e32 v2, s40, v223
	v_add_u32_e32 v6, s41, v223
	ds_read_b128 v[26:29], v2
	ds_read_b128 v[30:33], v2 offset:1024
	ds_read_b128 v[18:21], v2 offset:2048
	ds_read_b128 v[22:25], v2 offset:3072
	ds_read_b128 v[10:13], v6
	ds_read_b128 v[14:17], v6 offset:1024
	ds_read_b128 v[2:5], v6 offset:2048
	ds_read_b128 v[6:9], v6 offset:3072
	s_mov_b32 m0, s15
	ds_read_b128 v[34:37], v234 offset:32768
	ds_read_b128 v[38:41], v234 offset:33792
	ds_read_b128 v[42:45], v234 offset:34816
	ds_read_b128 v[46:49], v234 offset:35840
	ds_read_b128 v[50:53], v234 offset:36864
	ds_read_b128 v[54:57], v234 offset:37888
	ds_read_b128 v[58:61], v234 offset:38912
	ds_read_b128 v[62:65], v234 offset:39936
	global_load_lds_dwordx4 v66, s[4:5]
	s_mov_b32 m0, s16
	s_nop 0
	global_load_lds_dwordx4 v205, s[4:5]
	s_waitcnt vmcnt(8)
	s_waitcnt lgkmcnt(0)
	s_barrier
	s_setprio 1
	s_waitcnt lgkmcnt(0)
	v_mfma_scale_f32_16x16x128_f8f6f4 v[186:189], v[26:33], v[34:41], v[186:189], v216, v217 op_sel_hi:[0,0,0]
	v_mfma_scale_f32_16x16x128_f8f6f4 v[194:197], v[18:25], v[34:41], v[194:197], v216, v217 op_sel_hi:[0,0,0]
	v_mfma_scale_f32_16x16x128_f8f6f4 v[170:173], v[26:33], v[42:49], v[170:173], v216, v217 op_sel_hi:[0,0,0]
	v_mfma_scale_f32_16x16x128_f8f6f4 v[178:181], v[18:25], v[42:49], v[178:181], v216, v217 op_sel_hi:[0,0,0]
	v_mfma_scale_f32_16x16x128_f8f6f4 v[154:157], v[26:33], v[50:57], v[154:157], v216, v217 op_sel_hi:[0,0,0]
	v_mfma_scale_f32_16x16x128_f8f6f4 v[162:165], v[18:25], v[50:57], v[162:165], v216, v217 op_sel_hi:[0,0,0]
	v_mfma_scale_f32_16x16x128_f8f6f4 v[138:141], v[26:33], v[58:65], v[138:141], v216, v217 op_sel_hi:[0,0,0]
	v_mfma_scale_f32_16x16x128_f8f6f4 v[146:149], v[18:25], v[58:65], v[146:149], v216, v217 op_sel_hi:[0,0,0]
	s_setprio 0
	s_setprio 1
	v_mfma_scale_f32_16x16x128_f8f6f4 v[182:185], v[10:17], v[34:41], v[182:185], v216, v217 op_sel_hi:[0,0,0]
	v_mfma_scale_f32_16x16x128_f8f6f4 v[190:193], v[2:9], v[34:41], v[190:193], v216, v217 op_sel_hi:[0,0,0]
	v_mfma_scale_f32_16x16x128_f8f6f4 v[166:169], v[10:17], v[42:49], v[166:169], v216, v217 op_sel_hi:[0,0,0]
	v_mfma_scale_f32_16x16x128_f8f6f4 v[174:177], v[2:9], v[42:49], v[174:177], v216, v217 op_sel_hi:[0,0,0]
	v_mfma_scale_f32_16x16x128_f8f6f4 v[150:153], v[10:17], v[50:57], v[150:153], v216, v217 op_sel_hi:[0,0,0]
	v_mfma_scale_f32_16x16x128_f8f6f4 v[158:161], v[2:9], v[50:57], v[158:161], v216, v217 op_sel_hi:[0,0,0]
	v_mfma_scale_f32_16x16x128_f8f6f4 v[134:137], v[10:17], v[58:65], v[134:137], v216, v217 op_sel_hi:[0,0,0]
	v_mfma_scale_f32_16x16x128_f8f6f4 v[142:145], v[2:9], v[58:65], v[142:145], v216, v217 op_sel_hi:[0,0,0]
	s_setprio 0
	s_barrier
	s_add_i32 s4, s40, s10
	v_lshl_add_u64 v[214:215], v[214:215], 0, s[50:51]
	s_mov_b32 m0, s4
	ds_read_b128 v[58:61], v234 offset:49152
	ds_read_b128 v[62:65], v234 offset:50176
	ds_read_b128 v[50:53], v234 offset:51200
	ds_read_b128 v[54:57], v234 offset:52224
	ds_read_b128 v[42:45], v234 offset:53248
	ds_read_b128 v[46:49], v234 offset:54272
	ds_read_b128 v[34:37], v234 offset:55296
	ds_read_b128 v[38:41], v234 offset:56320
	global_load_lds_dwordx4 v[214:215], off
	s_add_i32 m0, s4, 0x2000
	s_add_u32 s4, s96, 0x20080
	v_lshl_add_u64 v[212:213], v[212:213], 0, s[50:51]
	s_addc_u32 s5, s97, 0
	s_add_i32 s40, s41, s10
	global_load_lds_dwordx4 v[212:213], off
	v_lshl_add_u64 v[212:213], s[4:5], 0, v[198:199]
	s_mov_b32 m0, s40
	v_lshl_add_u64 v[68:69], v[68:69], 0, s[50:51]
	global_load_lds_dwordx4 v[212:213], off
	v_lshl_add_u64 v[212:213], s[4:5], 0, v[200:201]
	s_add_i32 m0, s40, 0x2000
	s_and_b64 vcc, exec, s[42:43]
	global_load_lds_dwordx4 v[212:213], off
	v_lshl_add_u64 v[212:213], v[242:243], 0, s[50:51]
	s_mov_b32 m0, s7
	s_nop 0
	global_load_lds_dwordx4 v[212:213], off
	s_mov_b32 m0, s13
	s_nop 0
	global_load_lds_dwordx4 v[68:69], off
	s_waitcnt vmcnt(8)
	s_waitcnt lgkmcnt(0)
	s_barrier
	s_cbranch_vccnz .LBB0_953
	s_setprio 1
	s_waitcnt lgkmcnt(0)
	v_mfma_scale_f32_16x16x128_f8f6f4 v[118:121], v[26:33], v[58:65], v[118:121], v216, v217 op_sel_hi:[0,0,0]
	v_mfma_scale_f32_16x16x128_f8f6f4 v[126:129], v[18:25], v[58:65], v[126:129], v216, v217 op_sel_hi:[0,0,0]
	v_mfma_scale_f32_16x16x128_f8f6f4 v[102:105], v[26:33], v[50:57], v[102:105], v216, v217 op_sel_hi:[0,0,0]
	v_mfma_scale_f32_16x16x128_f8f6f4 v[110:113], v[18:25], v[50:57], v[110:113], v216, v217 op_sel_hi:[0,0,0]
	v_mfma_scale_f32_16x16x128_f8f6f4 v[86:89], v[26:33], v[42:49], v[86:89], v216, v217 op_sel_hi:[0,0,0]
	v_mfma_scale_f32_16x16x128_f8f6f4 v[94:97], v[18:25], v[42:49], v[94:97], v216, v217 op_sel_hi:[0,0,0]
	v_mfma_scale_f32_16x16x128_f8f6f4 v[70:73], v[26:33], v[34:41], v[70:73], v216, v217 op_sel_hi:[0,0,0]
	v_mfma_scale_f32_16x16x128_f8f6f4 v[78:81], v[18:25], v[34:41], v[78:81], v216, v217 op_sel_hi:[0,0,0]
	s_setprio 0
	s_setprio 1
	v_mfma_scale_f32_16x16x128_f8f6f4 v[122:125], v[10:17], v[58:65], v[122:125], v216, v217 op_sel_hi:[0,0,0]
	v_mfma_scale_f32_16x16x128_f8f6f4 v[130:133], v[2:9], v[58:65], v[130:133], v216, v217 op_sel_hi:[0,0,0]
	v_mfma_scale_f32_16x16x128_f8f6f4 v[106:109], v[10:17], v[50:57], v[106:109], v216, v217 op_sel_hi:[0,0,0]
	v_mfma_scale_f32_16x16x128_f8f6f4 v[114:117], v[2:9], v[50:57], v[114:117], v216, v217 op_sel_hi:[0,0,0]
	v_mfma_scale_f32_16x16x128_f8f6f4 v[90:93], v[10:17], v[42:49], v[90:93], v216, v217 op_sel_hi:[0,0,0]
	v_mfma_scale_f32_16x16x128_f8f6f4 v[98:101], v[2:9], v[42:49], v[98:101], v216, v217 op_sel_hi:[0,0,0]
	v_mfma_scale_f32_16x16x128_f8f6f4 v[74:77], v[10:17], v[34:41], v[74:77], v216, v217 op_sel_hi:[0,0,0]
	v_mfma_scale_f32_16x16x128_f8f6f4 v[82:85], v[2:9], v[34:41], v[82:85], v216, v217 op_sel_hi:[0,0,0]
	s_setprio 0
	s_branch .LBB0_953

; #define PG8_STAGE(bufoff, gbase, voff) do { _Pragma("unroll") for (int _i = 0; _i < 2; ++_i) \
;         __builtin_amdgcn_global_load_lds((const unsigned*)((const char*)(gbase) + (voff)[_i]), (LAS unsigned*)(lds + (bufoff) + ldsw + _i * 8192), 16, 0, 0); } while (0)
; #define PG8_LDA(dst, b, h) do { _Pragma("unroll") for (int m = 0; m < 4; ++m) _Pragma("unroll") for (int k = 0; k < 2; ++k) dst[m][k] = *(const LAS bf16x8*)(lds + PG8_SA(b, h) + aoff + m * 2048 + k * 1024); } while (0)
; #define PG8_LDB(dst, b, h) do { _Pragma("unroll") for (int n = 0; n < 2; ++n) _Pragma("unroll") for (int k = 0; k < 2; ++k) dst[n][k] = *(const LAS bf16x8*)(lds + PG8_SB(b, h) + boff + n * 2048 + k * 1024); } while (0)
; #define PG8_WAIT_V(n) asm volatile("s_waitcnt vmcnt(" #n ")" ::: "memory")
; #define PG8_WAIT_L(n) asm volatile("s_waitcnt lgkmcnt(" #n ")" ::: "memory")
; #define PG8_BAR __builtin_amdgcn_s_barrier()
; #define PG8_SCHED __builtin_amdgcn_sched_barrier(0)
;     ...
;             if constexpr (SP2) {
;             PG8_LDB(B0, 0, 0); PG8_LDB(B1, 0, 1); PG8_SCHED; PG8_LDA(At, 0, 0); PG8_STAGE(PG8_SA(1, 1), a1 + ah, VA1);
;             PG8_WAIT_V(8); PG8_WAIT_L(0); PG8_BAR; PG8_MMA(0, 0, At, B0); PG8_MMA(0, 1, At, B1); PG8_BAR; PG8_SCHED;
;             PG8_LDA(At, 0, 1); PG8_STAGE(PG8_SB(0, 0), b2, voffB); PG8_STAGE(PG8_SB(0, 1), b2 + bstep, voffB); PG8_STAGE(PG8_SA(0, 0), a2, v2[0]);
;             PG8_WAIT_V(8); PG8_WAIT_L(0); PG8_BAR; if (full) { PG8_MMA(1, 0, At, B0); PG8_MMA(1, 1, At, B1); } PG8_BAR; PG8_SCHED;
;             PG8_LDB(B0, 1, 0); PG8_LDB(B1, 1, 1); PG8_SCHED; PG8_LDA(At, 1, 0); PG8_STAGE(PG8_SA(0, 1), a2 + ah, v2[1]);
;             PG8_WAIT_V(8); PG8_WAIT_L(0); PG8_BAR; PG8_MMA(0, 0, At, B0); PG8_MMA(0, 1, At, B1); PG8_BAR; PG8_SCHED;
;             PG8_LDA(At, 1, 1); PG8_STAGE(PG8_SB(1, 0), b3, voffB); PG8_STAGE(PG8_SB(1, 1), b3 + bstep, voffB); PG8_STAGE(PG8_SA(1, 0), a3, v2[0]);
;             PG8_WAIT_V(8); PG8_WAIT_L(0); PG8_BAR; if (full) { PG8_MMA(1, 0, At, B0); PG8_MMA(1, 1, At, B1); } PG8_BAR; PG8_SCHED;
.LBB0_1068:
	s_add_u32 s4, s4, 0x8000
	s_addc_u32 s5, s5, 0
	s_barrier
	s_add_i32 s18, 0, 0x18000
	s_add_i32 s19, 0, 0x1c000
	v_add_u32_e32 v2, s18, v247
	v_add_u32_e32 v6, s19, v247
	ds_read_b128 v[26:29], v2
	ds_read_b128 v[30:33], v2 offset:1024
	ds_read_b128 v[18:21], v2 offset:2048
	ds_read_b128 v[22:25], v2 offset:3072
	ds_read_b128 v[10:13], v6
	ds_read_b128 v[14:17], v6 offset:1024
	ds_read_b128 v[2:5], v6 offset:2048
	ds_read_b128 v[6:9], v6 offset:3072
	s_mov_b32 m0, s14
	v_lshl_add_u64 v[250:251], s[4:5], 0, v[200:201]
	ds_read_b128 v[34:37], v223 offset:32768
	ds_read_b128 v[38:41], v223 offset:33792
	ds_read_b128 v[42:45], v223 offset:34816
	ds_read_b128 v[46:49], v223 offset:35840
	ds_read_b128 v[50:53], v223 offset:36864
	ds_read_b128 v[54:57], v223 offset:37888
	ds_read_b128 v[58:61], v223 offset:38912
	ds_read_b128 v[62:65], v223 offset:39936
	global_load_lds_dwordx4 v[250:251], off
	v_lshl_add_u64 v[250:251], s[4:5], 0, v[202:203]
	s_mov_b32 m0, s15
	s_nop 0
	global_load_lds_dwordx4 v[250:251], off
	s_waitcnt vmcnt(8)
	s_waitcnt lgkmcnt(0)
	s_barrier
	s_setprio 1
	s_waitcnt lgkmcnt(0)
	v_mfma_scale_f32_16x16x128_f8f6f4 v[172:175], v[26:33], v[34:41], v[172:175], v1, v246 op_sel_hi:[0,0,0]
	v_mfma_scale_f32_16x16x128_f8f6f4 v[176:179], v[18:25], v[34:41], v[176:179], v1, v246 op_sel_hi:[0,0,0]
	v_mfma_scale_f32_16x16x128_f8f6f4 v[168:171], v[26:33], v[42:49], v[168:171], v1, v246 op_sel_hi:[0,0,0]
	v_mfma_scale_f32_16x16x128_f8f6f4 v[164:167], v[18:25], v[42:49], v[164:167], v1, v246 op_sel_hi:[0,0,0]
	v_mfma_scale_f32_16x16x128_f8f6f4 v[144:147], v[26:33], v[50:57], v[144:147], v1, v246 op_sel_hi:[0,0,0]
	v_mfma_scale_f32_16x16x128_f8f6f4 v[136:139], v[18:25], v[50:57], v[136:139], v1, v246 op_sel_hi:[0,0,0]
	v_mfma_scale_f32_16x16x128_f8f6f4 v[116:119], v[26:33], v[58:65], v[116:119], v1, v246 op_sel_hi:[0,0,0]
	v_mfma_scale_f32_16x16x128_f8f6f4 v[112:115], v[18:25], v[58:65], v[112:115], v1, v246 op_sel_hi:[0,0,0]
	s_setprio 0
	s_setprio 1
	v_mfma_scale_f32_16x16x128_f8f6f4 v[188:191], v[10:17], v[34:41], v[188:191], v1, v246 op_sel_hi:[0,0,0]
	v_mfma_scale_f32_16x16x128_f8f6f4 v[192:195], v[2:9], v[34:41], v[192:195], v1, v246 op_sel_hi:[0,0,0]
	v_mfma_scale_f32_16x16x128_f8f6f4 v[184:187], v[10:17], v[42:49], v[184:187], v1, v246 op_sel_hi:[0,0,0]
	v_mfma_scale_f32_16x16x128_f8f6f4 v[180:183], v[2:9], v[42:49], v[180:183], v1, v246 op_sel_hi:[0,0,0]
	v_mfma_scale_f32_16x16x128_f8f6f4 v[152:155], v[10:17], v[50:57], v[152:155], v1, v246 op_sel_hi:[0,0,0]
	v_mfma_scale_f32_16x16x128_f8f6f4 v[148:151], v[2:9], v[50:57], v[148:151], v1, v246 op_sel_hi:[0,0,0]
	v_mfma_scale_f32_16x16x128_f8f6f4 v[120:123], v[10:17], v[58:65], v[120:123], v1, v246 op_sel_hi:[0,0,0]
	v_mfma_scale_f32_16x16x128_f8f6f4 v[80:83], v[2:9], v[58:65], v[80:83], v1, v246 op_sel_hi:[0,0,0]
	s_setprio 0
	s_barrier
	s_add_i32 s4, s18, s7
	v_lshl_add_u64 v[250:251], v[240:241], 0, s[48:49]
	s_mov_b32 m0, s4
	ds_read_b128 v[58:61], v223 offset:49152
	ds_read_b128 v[62:65], v223 offset:50176
	ds_read_b128 v[50:53], v223 offset:51200
	ds_read_b128 v[54:57], v223 offset:52224
	ds_read_b128 v[42:45], v223 offset:53248
	ds_read_b128 v[46:49], v223 offset:54272
	ds_read_b128 v[34:37], v223 offset:55296
	ds_read_b128 v[38:41], v223 offset:56320
	global_load_lds_dwordx4 v[250:251], off
	v_lshl_add_u64 v[250:251], v[238:239], 0, s[48:49]
	s_add_i32 m0, s4, 0x2000
	s_add_i32 s4, s19, s7
	global_load_lds_dwordx4 v[250:251], off
	v_lshl_add_u64 v[240:241], v[240:241], 0, s[50:51]
	s_mov_b32 m0, s4
	v_lshl_add_u64 v[238:239], v[238:239], 0, s[50:51]
	global_load_lds_dwordx4 v[240:241], off
	s_add_i32 m0, s4, 0x2000
	s_andn2_b64 vcc, exec, s[88:89]
	global_load_lds_dwordx4 v[238:239], off
	v_lshl_add_u64 v[238:239], v[242:243], 0, s[48:49]
	s_mov_b32 m0, s21
	s_nop 0
	global_load_lds_dwordx4 v[238:239], off
	v_lshl_add_u64 v[238:239], v[244:245], 0, s[48:49]
	s_mov_b32 m0, s22
	s_nop 0
	global_load_lds_dwordx4 v[238:239], off
	s_waitcnt vmcnt(8)
	s_waitcnt lgkmcnt(0)
	s_barrier
	s_cbranch_vccnz .LBB0_1070
	s_setprio 1
	s_waitcnt lgkmcnt(0)
	v_mfma_scale_f32_16x16x128_f8f6f4 v[128:131], v[26:33], v[58:65], v[128:131], v1, v246 op_sel_hi:[0,0,0]
	v_mfma_scale_f32_16x16x128_f8f6f4 v[124:127], v[18:25], v[58:65], v[124:127], v1, v246 op_sel_hi:[0,0,0]
	v_mfma_scale_f32_16x16x128_f8f6f4 v[108:111], v[26:33], v[50:57], v[108:111], v1, v246 op_sel_hi:[0,0,0]
	v_mfma_scale_f32_16x16x128_f8f6f4 v[104:107], v[18:25], v[50:57], v[104:107], v1, v246 op_sel_hi:[0,0,0]
	v_mfma_scale_f32_16x16x128_f8f6f4 v[92:95], v[26:33], v[42:49], v[92:95], v1, v246 op_sel_hi:[0,0,0]
	v_mfma_scale_f32_16x16x128_f8f6f4 v[84:87], v[18:25], v[42:49], v[84:87], v1, v246 op_sel_hi:[0,0,0]
	v_mfma_scale_f32_16x16x128_f8f6f4 v[76:79], v[26:33], v[34:41], v[76:79], v1, v246 op_sel_hi:[0,0,0]
	v_mfma_scale_f32_16x16x128_f8f6f4 v[72:75], v[18:25], v[34:41], v[72:75], v1, v246 op_sel_hi:[0,0,0]
	s_setprio 0
	s_setprio 1
	v_mfma_scale_f32_16x16x128_f8f6f4 v[160:163], v[10:17], v[58:65], v[160:163], v1, v246 op_sel_hi:[0,0,0]
	v_mfma_scale_f32_16x16x128_f8f6f4 v[156:159], v[2:9], v[58:65], v[156:159], v1, v246 op_sel_hi:[0,0,0]
	v_mfma_scale_f32_16x16x128_f8f6f4 v[140:143], v[10:17], v[50:57], v[140:143], v1, v246 op_sel_hi:[0,0,0]
	v_mfma_scale_f32_16x16x128_f8f6f4 v[132:135], v[2:9], v[50:57], v[132:135], v1, v246 op_sel_hi:[0,0,0]
	v_mfma_scale_f32_16x16x128_f8f6f4 v[100:103], v[10:17], v[42:49], v[100:103], v1, v246 op_sel_hi:[0,0,0]
	v_mfma_scale_f32_16x16x128_f8f6f4 v[96:99], v[2:9], v[42:49], v[96:99], v1, v246 op_sel_hi:[0,0,0]
	v_mfma_scale_f32_16x16x128_f8f6f4 v[88:91], v[10:17], v[34:41], v[88:91], v1, v246 op_sel_hi:[0,0,0]
	v_mfma_scale_f32_16x16x128_f8f6f4 v[68:71], v[2:9], v[34:41], v[68:71], v1, v246 op_sel_hi:[0,0,0]
	s_setprio 0
